# retention out pass output loop: division and scaling chains as packed-f32 ops (v_pk_fma/mul/add with neg modifiers), same per-element operations
# speedup vs baseline: 1.0066x; 1.0066x over previous
; #define LAS __attribute__((address_space(3)))
; __device__ __forceinline__ bf16_t f2bf(float f) { unsigned u = __builtin_bit_cast(unsigned, f); return (bf16_t)((u + 0x7fffu + ((u >> 16) & 1u)) >> 16); }
; __device__ __forceinline__ int crow(int r, int hi) { return (r & 3) + 8 * (r >> 2) + 4 * hi; }
; __device__ __forceinline__ int crow(int r, int hi) { return (r & 3) + 8 * (r >> 2) + 4 * hi; }
; template <int DK, int DV, bool MLSTM>
; __device__ __forceinline__ void out_unit2(LAS unsigned char* lds, LAS unsigned char* ldstab, const OutArgs a, const int wv) {
;     ...
;     for (int r = 0; r < 16; ++r) {
;         const int row = 32 * rb + crow(r, hi);
;         const float t1 = s1[r] + exch[((1 - dh) * 128 + row) * 2], t2 = s2[r] + exch[((1 - dh) * 128 + row) * 2 + 1];
;         float mean, inv;
;         if (MLSTM) { mean = 0.f; inv = rsqrtf(t2 * (1.f / DV) + EPS); }
;         else { mean = t1 * (1.f / DV); inv = rsqrtf(fmaxf(t2 * (1.f / DV) - mean * mean, 0.f) + EPS); }
; #pragma unroll
;         for (int nb = 0; nb < NB; ++nb) { const int col = dh * (DV / 2) + 32 * nb + r32;
;             *(LAS bf16_t*)(lds + row * TP + col * 2) = f2bf((o[nb][r] - mean) * inv); }
;     }
.LBB0_1838:
	s_or_b64 exec, exec, s[4:5]
	v_lshlrev_b32_e32 v164, 1, v219
	v_subrev_u32_e32 v164, s6, v164
	s_add_i32 s4, 0, 0x22100
	v_lshl_add_u32 v164, v164, 2, s4
	s_waitcnt vmcnt(0) lgkmcnt(0)
	s_barrier
	ds_read_b128 v[164:167], v164 offset:1024
	v_lshlrev_b32_e32 v168, 1, v217
	v_subrev_u32_e32 v168, s6, v168
	v_lshl_add_u32 v168, v168, 2, s4
	ds_read2_b64 v[168:171], v168 offset0:128 offset1:129
	s_waitcnt lgkmcnt(1)
	v_pk_add_f32 v[156:157], v[156:157], v[164:165]
	s_nop 0
	v_pk_mul_f32 v[156:157], v[156:157], s[36:37] op_sel_hi:[1,0]
	s_nop 0
	v_fma_f32 v157, -v156, v156, v157
	v_max_f32_e32 v157, 0, v157
	v_add_f32_e32 v157, 0x358637bd, v157
	v_mul_f32_e32 v164, 0x4b800000, v157
	v_cmp_gt_f32_e32 vcc, s89, v157
	v_sub_f32_e32 v16, v16, v156
	v_sub_f32_e32 v0, v0, v156
	v_cndmask_b32_e32 v157, v157, v164, vcc
	v_rsq_f32_e32 v157, v157
	v_or_b32_e32 v164, s6, v233
	v_mul_f32_e32 v165, 0x45800000, v157
	v_cndmask_b32_e32 v157, v157, v165, vcc
	v_mul_f32_e32 v16, v16, v157
	v_bfe_u32 v172, v16, 16, 1
	v_lshlrev_b32_e32 v165, 10, v219
	v_add3_u32 v172, v16, v172, s90
	v_lshlrev_b32_e32 v16, 1, v164
	v_mul_f32_e32 v0, v0, v157
	v_add3_u32 v164, 0, v165, v16
	v_bfe_u32 v165, v0, 16, 1
	v_add3_u32 v0, v0, v165, s90
	ds_write_b16_d16_hi v164, v0 offset:64
	v_sub_f32_e32 v0, v32, v156
	v_mul_f32_e32 v0, v0, v157
	v_bfe_u32 v32, v0, 16, 1
	v_add3_u32 v0, v0, v32, s90
	ds_write_b16_d16_hi v164, v0 offset:128
	v_sub_f32_e32 v0, v48, v156
	v_mul_f32_e32 v0, v0, v157
	v_bfe_u32 v32, v0, 16, 1
	v_add3_u32 v0, v0, v32, s90
	ds_write_b16_d16_hi v164, v0 offset:192
	v_sub_f32_e32 v0, v96, v156
	v_mul_f32_e32 v0, v0, v157
	v_bfe_u32 v32, v0, 16, 1
	v_add3_u32 v0, v0, v32, s90
	ds_write_b16_d16_hi v164, v0 offset:256
	v_sub_f32_e32 v0, v112, v156
	v_mul_f32_e32 v0, v0, v157
	v_bfe_u32 v32, v0, 16, 1
	v_add3_u32 v0, v0, v32, s90
	ds_write_b16_d16_hi v164, v0 offset:320
	v_sub_f32_e32 v0, v80, v156
	v_mul_f32_e32 v0, v0, v157
	v_bfe_u32 v32, v0, 16, 1
	v_add3_u32 v0, v0, v32, s90
	ds_write_b16_d16_hi v164, v0 offset:384
	v_sub_f32_e32 v0, v64, v156
	v_mul_f32_e32 v0, v0, v157
	v_pk_add_f32 v[156:157], v[158:159], v[166:167]
	ds_write_b16_d16_hi v164, v172
	v_pk_mul_f32 v[156:157], v[156:157], s[36:37] op_sel_hi:[1,0]
	s_nop 0
	v_fma_f32 v32, -v156, v156, v157
	v_max_f32_e32 v32, 0, v32
	v_add_f32_e32 v32, 0x358637bd, v32
	v_mul_f32_e32 v48, 0x4b800000, v32
	v_cmp_gt_f32_e32 vcc, s89, v32
	v_sub_f32_e32 v17, v17, v156
	v_sub_f32_e32 v1, v1, v156
	v_cndmask_b32_e32 v32, v32, v48, vcc
	v_rsq_f32_e32 v32, v32
	v_bfe_u32 v48, v0, 16, 1
	v_add3_u32 v0, v0, v48, s90
	ds_write_b16_d16_hi v164, v0 offset:448
	v_mul_f32_e32 v0, 0x45800000, v32
	v_cndmask_b32_e32 v0, v32, v0, vcc
	v_mul_f32_e32 v17, v17, v0
	v_lshlrev_b32_e32 v32, 10, v218
	v_bfe_u32 v48, v17, 16, 1
	v_add3_u32 v17, v17, v48, s90
	v_add3_u32 v32, 0, v32, v16
	v_mul_f32_e32 v1, v1, v0
	ds_write_b16_d16_hi v32, v17
	v_bfe_u32 v17, v1, 16, 1
	v_add3_u32 v1, v1, v17, s90
	ds_write_b16_d16_hi v32, v1 offset:64
	v_sub_f32_e32 v1, v33, v156
	v_mul_f32_e32 v1, v1, v0
	v_bfe_u32 v17, v1, 16, 1
	v_add3_u32 v1, v1, v17, s90
	ds_write_b16_d16_hi v32, v1 offset:128
	v_sub_f32_e32 v1, v49, v156
	v_mul_f32_e32 v1, v1, v0
	v_bfe_u32 v17, v1, 16, 1
	v_add3_u32 v1, v1, v17, s90
	ds_write_b16_d16_hi v32, v1 offset:192
	v_sub_f32_e32 v1, v97, v156
	v_mul_f32_e32 v1, v1, v0
	v_bfe_u32 v17, v1, 16, 1
	v_add3_u32 v1, v1, v17, s90
	ds_write_b16_d16_hi v32, v1 offset:256
	v_sub_f32_e32 v1, v113, v156
	v_mul_f32_e32 v1, v1, v0
	v_bfe_u32 v17, v1, 16, 1
	v_add3_u32 v1, v1, v17, s90
	ds_write_b16_d16_hi v32, v1 offset:320
	v_sub_f32_e32 v1, v81, v156
	v_mul_f32_e32 v1, v1, v0
	v_bfe_u32 v17, v1, 16, 1
	v_add3_u32 v1, v1, v17, s90
	ds_write_b16_d16_hi v32, v1 offset:384
	v_sub_f32_e32 v1, v65, v156
	v_mul_f32_e32 v17, v1, v0
	s_waitcnt lgkmcnt(14)
	v_pk_add_f32 v[0:1], v[152:153], v[168:169]
	s_nop 0
	v_pk_mul_f32 v[0:1], v[0:1], s[36:37] op_sel_hi:[1,0]
	s_nop 0
	v_fma_f32 v1, -v0, v0, v1
	v_max_f32_e32 v1, 0, v1
	v_add_f32_e32 v1, 0x358637bd, v1
	v_mul_f32_e32 v33, 0x4b800000, v1
	v_cmp_gt_f32_e32 vcc, s89, v1
	v_sub_f32_e32 v18, v18, v0
	v_sub_f32_e32 v2, v2, v0
	v_cndmask_b32_e32 v1, v1, v33, vcc
	v_rsq_f32_e32 v1, v1
	v_bfe_u32 v33, v17, 16, 1
	v_add3_u32 v17, v17, v33, s90
	ds_write_b16_d16_hi v32, v17 offset:448
	v_mul_f32_e32 v17, 0x45800000, v1
	v_cndmask_b32_e32 v1, v1, v17, vcc
	v_mul_f32_e32 v18, v18, v1
	v_lshlrev_b32_e32 v17, 10, v217
	v_bfe_u32 v32, v18, 16, 1
	v_add3_u32 v18, v18, v32, s90
	v_add3_u32 v17, 0, v17, v16
	v_mul_f32_e32 v2, v2, v1
	ds_write_b16_d16_hi v17, v18
	v_bfe_u32 v18, v2, 16, 1
	v_add3_u32 v2, v2, v18, s90
	ds_write_b16_d16_hi v17, v2 offset:64
	v_sub_f32_e32 v2, v34, v0
	v_mul_f32_e32 v2, v2, v1
	v_bfe_u32 v18, v2, 16, 1
	v_add3_u32 v2, v2, v18, s90
	ds_write_b16_d16_hi v17, v2 offset:128
	v_sub_f32_e32 v2, v50, v0
	v_mul_f32_e32 v2, v2, v1
	v_bfe_u32 v18, v2, 16, 1
	v_add3_u32 v2, v2, v18, s90
	ds_write_b16_d16_hi v17, v2 offset:192
	v_sub_f32_e32 v2, v98, v0
	v_mul_f32_e32 v2, v2, v1
	v_bfe_u32 v18, v2, 16, 1
	v_add3_u32 v2, v2, v18, s90
	ds_write_b16_d16_hi v17, v2 offset:256
	v_sub_f32_e32 v2, v114, v0
	v_mul_f32_e32 v2, v2, v1
	v_bfe_u32 v18, v2, 16, 1
	v_add3_u32 v2, v2, v18, s90
	ds_write_b16_d16_hi v17, v2 offset:320
	v_sub_f32_e32 v2, v82, v0
	v_mul_f32_e32 v2, v2, v1
	v_bfe_u32 v18, v2, 16, 1
	v_add3_u32 v2, v2, v18, s90
	v_sub_f32_e32 v0, v66, v0
	ds_write_b16_d16_hi v17, v2 offset:384
	v_mul_f32_e32 v2, v0, v1
	v_pk_add_f32 v[0:1], v[154:155], v[170:171]
	s_nop 0
	v_pk_mul_f32 v[0:1], v[0:1], s[36:37] op_sel_hi:[1,0]
	s_nop 0
	v_fma_f32 v1, -v0, v0, v1
	v_max_f32_e32 v1, 0, v1
; #define LAS __attribute__((address_space(3)))
; __device__ __forceinline__ bf16_t f2bf(float f) { unsigned u = __builtin_bit_cast(unsigned, f); return (bf16_t)((u + 0x7fffu + ((u >> 16) & 1u)) >> 16); }
; __device__ __forceinline__ int crow(int r, int hi) { return (r & 3) + 8 * (r >> 2) + 4 * hi; }
; __device__ __forceinline__ int crow(int r, int hi) { return (r & 3) + 8 * (r >> 2) + 4 * hi; }
; template <int DK, int DV, bool MLSTM>
; __device__ __forceinline__ void out_unit2(LAS unsigned char* lds, LAS unsigned char* ldstab, const OutArgs a, const int wv) {
;     ...
;     for (int r = 0; r < 16; ++r) {
;         const int row = 32 * rb + crow(r, hi);
;         const float t1 = s1[r] + exch[((1 - dh) * 128 + row) * 2], t2 = s2[r] + exch[((1 - dh) * 128 + row) * 2 + 1];
;         float mean, inv;
;         if (MLSTM) { mean = 0.f; inv = rsqrtf(t2 * (1.f / DV) + EPS); }
;         else { mean = t1 * (1.f / DV); inv = rsqrtf(fmaxf(t2 * (1.f / DV) - mean * mean, 0.f) + EPS); }
; #pragma unroll
;         for (int nb = 0; nb < NB; ++nb) { const int col = dh * (DV / 2) + 32 * nb + r32;
;             *(LAS bf16_t*)(lds + row * TP + col * 2) = f2bf((o[nb][r] - mean) * inv); }
;     }
	v_add_f32_e32 v1, 0x358637bd, v1
	v_mul_f32_e32 v18, 0x4b800000, v1
	v_cmp_gt_f32_e32 vcc, s89, v1
	s_nop 1
	v_cndmask_b32_e32 v1, v1, v18, vcc
	v_rsq_f32_e32 v1, v1
	v_bfe_u32 v18, v2, 16, 1
	v_add3_u32 v2, v2, v18, s90
	ds_write_b16_d16_hi v17, v2 offset:448
	v_mul_f32_e32 v2, 0x45800000, v1
	v_cndmask_b32_e32 v1, v1, v2, vcc
	v_sub_f32_e32 v17, v19, v0
	v_mul_f32_e32 v17, v17, v1
	v_lshlrev_b32_e32 v2, 10, v216
	v_bfe_u32 v18, v17, 16, 1
	v_add3_u32 v17, v17, v18, s90
	v_add3_u32 v18, 0, v2, v16
	v_sub_f32_e32 v2, v3, v0
	v_mul_f32_e32 v2, v2, v1
	v_bfe_u32 v3, v2, 16, 1
	v_add3_u32 v2, v2, v3, s90
	ds_write_b16_d16_hi v18, v2 offset:64
	v_sub_f32_e32 v2, v35, v0
	v_mul_f32_e32 v2, v2, v1
	v_bfe_u32 v3, v2, 16, 1
	v_add3_u32 v2, v2, v3, s90
	ds_write_b16_d16_hi v18, v2 offset:128
	v_sub_f32_e32 v2, v51, v0
	v_mul_f32_e32 v2, v2, v1
	v_bfe_u32 v3, v2, 16, 1
	v_add3_u32 v2, v2, v3, s90
	ds_write_b16_d16_hi v18, v2 offset:192
	v_sub_f32_e32 v2, v99, v0
	v_mul_f32_e32 v2, v2, v1
	v_bfe_u32 v3, v2, 16, 1
	v_add3_u32 v2, v2, v3, s90
	ds_write_b16_d16_hi v18, v2 offset:256
	v_sub_f32_e32 v2, v115, v0
	v_mul_f32_e32 v2, v2, v1
	v_bfe_u32 v3, v2, 16, 1
	v_add3_u32 v2, v2, v3, s90
	ds_write_b16_d16_hi v18, v2 offset:320
	v_sub_f32_e32 v2, v83, v0
	v_sub_f32_e32 v0, v67, v0
	ds_write_b16_d16_hi v18, v17
	v_mul_f32_e32 v2, v2, v1
	v_mul_f32_e32 v17, v0, v1
	v_lshlrev_b32_e32 v0, 1, v215
	v_bfe_u32 v3, v2, 16, 1
	v_subrev_u32_e32 v0, s6, v0
	v_add3_u32 v2, v2, v3, s90
	v_lshl_add_u32 v0, v0, 2, s4
	ds_write_b16_d16_hi v18, v2 offset:384
	ds_read2_b64 v[0:3], v0 offset0:128 offset1:129
	v_lshlrev_b32_e32 v19, 1, v213
	v_subrev_u32_e32 v19, s6, v19
	v_lshl_add_u32 v19, v19, 2, s4
	ds_read2_b64 v[32:35], v19 offset0:128 offset1:129
	s_waitcnt lgkmcnt(1)
	v_pk_add_f32 v[0:1], v[148:149], v[0:1]
	s_nop 0
	v_pk_mul_f32 v[0:1], v[0:1], s[36:37] op_sel_hi:[1,0]
	s_nop 0
	v_fma_f32 v1, -v0, v0, v1
	v_max_f32_e32 v1, 0, v1
	v_add_f32_e32 v1, 0x358637bd, v1
	v_mul_f32_e32 v19, 0x4b800000, v1
	v_cmp_gt_f32_e32 vcc, s89, v1
	v_sub_f32_e32 v4, v4, v0
	s_nop 0
	v_cndmask_b32_e32 v1, v1, v19, vcc
	v_rsq_f32_e32 v1, v1
	v_bfe_u32 v19, v17, 16, 1
	v_add3_u32 v17, v17, v19, s90
	ds_write_b16_d16_hi v18, v17 offset:448
	v_mul_f32_e32 v17, 0x45800000, v1
	v_cndmask_b32_e32 v1, v1, v17, vcc
	v_sub_f32_e32 v18, v20, v0
	v_mul_f32_e32 v18, v18, v1
	v_lshlrev_b32_e32 v17, 10, v215
	v_bfe_u32 v19, v18, 16, 1
	v_add3_u32 v18, v18, v19, s90
	v_add3_u32 v17, 0, v17, v16
	v_mul_f32_e32 v4, v4, v1
	ds_write_b16_d16_hi v17, v18
	v_bfe_u32 v18, v4, 16, 1
	v_add3_u32 v4, v4, v18, s90
	ds_write_b16_d16_hi v17, v4 offset:64
	v_sub_f32_e32 v4, v36, v0
	v_mul_f32_e32 v4, v4, v1
	v_bfe_u32 v18, v4, 16, 1
	v_add3_u32 v4, v4, v18, s90
	ds_write_b16_d16_hi v17, v4 offset:128
	v_sub_f32_e32 v4, v52, v0
	v_mul_f32_e32 v4, v4, v1
	v_bfe_u32 v18, v4, 16, 1
	v_add3_u32 v4, v4, v18, s90
	ds_write_b16_d16_hi v17, v4 offset:192
	v_sub_f32_e32 v4, v100, v0
	v_mul_f32_e32 v4, v4, v1
	v_bfe_u32 v18, v4, 16, 1
	v_add3_u32 v4, v4, v18, s90
	ds_write_b16_d16_hi v17, v4 offset:256
	v_sub_f32_e32 v4, v116, v0
	v_mul_f32_e32 v4, v4, v1
	v_bfe_u32 v18, v4, 16, 1
	v_add3_u32 v4, v4, v18, s90
	ds_write_b16_d16_hi v17, v4 offset:320
	v_sub_f32_e32 v4, v84, v0
	v_mul_f32_e32 v4, v4, v1
	v_bfe_u32 v18, v4, 16, 1
	v_add3_u32 v4, v4, v18, s90
	v_sub_f32_e32 v0, v68, v0
	ds_write_b16_d16_hi v17, v4 offset:384
	v_mul_f32_e32 v4, v0, v1
	v_pk_add_f32 v[0:1], v[150:151], v[2:3]
	s_nop 0
	v_pk_mul_f32 v[0:1], v[0:1], s[36:37] op_sel_hi:[1,0]
	s_nop 0
	v_fma_f32 v1, -v0, v0, v1
	v_max_f32_e32 v1, 0, v1
	v_add_f32_e32 v1, 0x358637bd, v1
	v_mul_f32_e32 v2, 0x4b800000, v1
	v_cmp_gt_f32_e32 vcc, s89, v1
	v_sub_f32_e32 v3, v21, v0
	s_nop 0
	v_cndmask_b32_e32 v1, v1, v2, vcc
	v_rsq_f32_e32 v1, v1
	v_bfe_u32 v2, v4, 16, 1
	v_add3_u32 v2, v4, v2, s90
	ds_write_b16_d16_hi v17, v2 offset:448
	v_mul_f32_e32 v2, 0x45800000, v1
	v_cndmask_b32_e32 v1, v1, v2, vcc
	v_mul_f32_e32 v3, v3, v1
	v_lshlrev_b32_e32 v2, 10, v214
	v_bfe_u32 v4, v3, 16, 1
	v_add3_u32 v3, v3, v4, s90
	v_add3_u32 v2, 0, v2, v16
	ds_write_b16_d16_hi v2, v3
	v_sub_f32_e32 v3, v5, v0
	v_mul_f32_e32 v3, v3, v1
	v_bfe_u32 v4, v3, 16, 1
	v_add3_u32 v3, v3, v4, s90
	ds_write_b16_d16_hi v2, v3 offset:64
	v_sub_f32_e32 v3, v37, v0
	v_mul_f32_e32 v3, v3, v1
	v_bfe_u32 v4, v3, 16, 1
	v_add3_u32 v3, v3, v4, s90
	ds_write_b16_d16_hi v2, v3 offset:128
	v_sub_f32_e32 v3, v53, v0
	v_mul_f32_e32 v3, v3, v1
	v_bfe_u32 v4, v3, 16, 1
	v_add3_u32 v3, v3, v4, s90
	ds_write_b16_d16_hi v2, v3 offset:192
	v_sub_f32_e32 v3, v101, v0
	v_mul_f32_e32 v3, v3, v1
	v_bfe_u32 v4, v3, 16, 1
	v_add3_u32 v3, v3, v4, s90
	ds_write_b16_d16_hi v2, v3 offset:256
	v_sub_f32_e32 v3, v117, v0
	v_mul_f32_e32 v3, v3, v1
	v_bfe_u32 v4, v3, 16, 1
	v_add3_u32 v3, v3, v4, s90
	ds_write_b16_d16_hi v2, v3 offset:320
	v_sub_f32_e32 v3, v85, v0
	v_mul_f32_e32 v3, v3, v1
	v_bfe_u32 v4, v3, 16, 1
	v_add3_u32 v3, v3, v4, s90
	v_sub_f32_e32 v0, v69, v0
	ds_write_b16_d16_hi v2, v3 offset:384
	v_mul_f32_e32 v3, v0, v1
	s_waitcnt lgkmcnt(14)
; #define LAS __attribute__((address_space(3)))
; __device__ __forceinline__ bf16_t f2bf(float f) { unsigned u = __builtin_bit_cast(unsigned, f); return (bf16_t)((u + 0x7fffu + ((u >> 16) & 1u)) >> 16); }
; __device__ __forceinline__ int crow(int r, int hi) { return (r & 3) + 8 * (r >> 2) + 4 * hi; }
; __device__ __forceinline__ int crow(int r, int hi) { return (r & 3) + 8 * (r >> 2) + 4 * hi; }
; template <int DK, int DV, bool MLSTM>
; __device__ __forceinline__ void out_unit2(LAS unsigned char* lds, LAS unsigned char* ldstab, const OutArgs a, const int wv) {
;     ...
;     for (int r = 0; r < 16; ++r) {
;         const int row = 32 * rb + crow(r, hi);
;         const float t1 = s1[r] + exch[((1 - dh) * 128 + row) * 2], t2 = s2[r] + exch[((1 - dh) * 128 + row) * 2 + 1];
;         float mean, inv;
;         if (MLSTM) { mean = 0.f; inv = rsqrtf(t2 * (1.f / DV) + EPS); }
;         else { mean = t1 * (1.f / DV); inv = rsqrtf(fmaxf(t2 * (1.f / DV) - mean * mean, 0.f) + EPS); }
; #pragma unroll
;         for (int nb = 0; nb < NB; ++nb) { const int col = dh * (DV / 2) + 32 * nb + r32;
;             *(LAS bf16_t*)(lds + row * TP + col * 2) = f2bf((o[nb][r] - mean) * inv); }
;     }
	v_pk_add_f32 v[0:1], v[144:145], v[32:33]
	s_nop 0
	v_pk_mul_f32 v[0:1], v[0:1], s[36:37] op_sel_hi:[1,0]
	s_nop 0
	v_fma_f32 v1, -v0, v0, v1
	v_max_f32_e32 v1, 0, v1
	v_add_f32_e32 v1, 0x358637bd, v1
	v_mul_f32_e32 v4, 0x4b800000, v1
	v_cmp_gt_f32_e32 vcc, s89, v1
	s_nop 1
	v_cndmask_b32_e32 v1, v1, v4, vcc
	v_rsq_f32_e32 v1, v1
	v_bfe_u32 v4, v3, 16, 1
	v_add3_u32 v3, v3, v4, s90
	ds_write_b16_d16_hi v2, v3 offset:448
	v_mul_f32_e32 v2, 0x45800000, v1
	v_cndmask_b32_e32 v1, v1, v2, vcc
	v_sub_f32_e32 v3, v22, v0
	v_mul_f32_e32 v3, v3, v1
	v_lshlrev_b32_e32 v2, 10, v213
	v_bfe_u32 v4, v3, 16, 1
	v_add3_u32 v3, v3, v4, s90
	v_add3_u32 v2, 0, v2, v16
	ds_write_b16_d16_hi v2, v3
	v_sub_f32_e32 v3, v6, v0
	v_mul_f32_e32 v3, v3, v1
	v_bfe_u32 v4, v3, 16, 1
	v_add3_u32 v3, v3, v4, s90
	ds_write_b16_d16_hi v2, v3 offset:64
	v_sub_f32_e32 v3, v38, v0
	v_mul_f32_e32 v3, v3, v1
	v_bfe_u32 v4, v3, 16, 1
	v_add3_u32 v3, v3, v4, s90
	ds_write_b16_d16_hi v2, v3 offset:128
	v_sub_f32_e32 v3, v54, v0
	v_mul_f32_e32 v3, v3, v1
	v_bfe_u32 v4, v3, 16, 1
	v_add3_u32 v3, v3, v4, s90
	ds_write_b16_d16_hi v2, v3 offset:192
	v_sub_f32_e32 v3, v102, v0
	v_mul_f32_e32 v3, v3, v1
	v_bfe_u32 v4, v3, 16, 1
	v_add3_u32 v3, v3, v4, s90
	ds_write_b16_d16_hi v2, v3 offset:256
	v_sub_f32_e32 v3, v118, v0
	v_mul_f32_e32 v3, v3, v1
	v_bfe_u32 v4, v3, 16, 1
	v_add3_u32 v3, v3, v4, s90
	ds_write_b16_d16_hi v2, v3 offset:320
	v_sub_f32_e32 v3, v86, v0
	v_mul_f32_e32 v3, v3, v1
	v_bfe_u32 v4, v3, 16, 1
	v_add3_u32 v3, v3, v4, s90
	v_sub_f32_e32 v0, v70, v0
	ds_write_b16_d16_hi v2, v3 offset:384
	v_mul_f32_e32 v3, v0, v1
	v_pk_add_f32 v[0:1], v[146:147], v[34:35]
	s_nop 0
	v_pk_mul_f32 v[0:1], v[0:1], s[36:37] op_sel_hi:[1,0]
	s_nop 0
	v_fma_f32 v1, -v0, v0, v1
	v_max_f32_e32 v1, 0, v1
	v_add_f32_e32 v1, 0x358637bd, v1
	v_mul_f32_e32 v4, 0x4b800000, v1
	v_cmp_gt_f32_e32 vcc, s89, v1
	s_nop 1
	v_cndmask_b32_e32 v1, v1, v4, vcc
	v_rsq_f32_e32 v1, v1
	v_bfe_u32 v4, v3, 16, 1
	v_add3_u32 v3, v3, v4, s90
	ds_write_b16_d16_hi v2, v3 offset:448
	v_mul_f32_e32 v2, 0x45800000, v1
	v_cndmask_b32_e32 v1, v1, v2, vcc
	v_sub_f32_e32 v3, v23, v0
	v_lshlrev_b32_e32 v2, 10, v212
	v_mul_f32_e32 v3, v3, v1
	v_bfe_u32 v4, v3, 16, 1
	v_add3_u32 v17, 0, v2, v16
	v_sub_f32_e32 v2, v7, v0
	v_add3_u32 v3, v3, v4, s90
	v_mul_f32_e32 v2, v2, v1
	ds_write_b16_d16_hi v17, v3
	v_bfe_u32 v3, v2, 16, 1
	v_add3_u32 v2, v2, v3, s90
	ds_write_b16_d16_hi v17, v2 offset:64
	v_sub_f32_e32 v2, v39, v0
	v_mul_f32_e32 v2, v2, v1
	v_bfe_u32 v3, v2, 16, 1
	v_add3_u32 v2, v2, v3, s90
	ds_write_b16_d16_hi v17, v2 offset:128
	v_sub_f32_e32 v2, v55, v0
	v_mul_f32_e32 v2, v2, v1
	v_bfe_u32 v3, v2, 16, 1
	v_add3_u32 v2, v2, v3, s90
	ds_write_b16_d16_hi v17, v2 offset:192
	v_sub_f32_e32 v2, v103, v0
	v_mul_f32_e32 v2, v2, v1
	v_bfe_u32 v3, v2, 16, 1
	v_add3_u32 v2, v2, v3, s90
	ds_write_b16_d16_hi v17, v2 offset:256
	v_sub_f32_e32 v2, v119, v0
	v_mul_f32_e32 v2, v2, v1
	v_bfe_u32 v3, v2, 16, 1
	v_add3_u32 v2, v2, v3, s90
	ds_write_b16_d16_hi v17, v2 offset:320
	v_sub_f32_e32 v2, v87, v0
	v_sub_f32_e32 v0, v71, v0
	v_mul_f32_e32 v2, v2, v1
	v_mul_f32_e32 v18, v0, v1
	v_lshlrev_b32_e32 v0, 1, v211
	v_bfe_u32 v3, v2, 16, 1
	v_subrev_u32_e32 v0, s6, v0
	v_add3_u32 v2, v2, v3, s90
	v_lshl_add_u32 v0, v0, 2, s4
	ds_write_b16_d16_hi v17, v2 offset:384
	ds_read2_b64 v[0:3], v0 offset0:128 offset1:129
	v_lshlrev_b32_e32 v4, 1, v209
	v_subrev_u32_e32 v4, s6, v4
	v_lshl_add_u32 v4, v4, 2, s4
	ds_read2_b64 v[4:7], v4 offset0:128 offset1:129
	s_waitcnt lgkmcnt(1)
	v_pk_add_f32 v[0:1], v[140:141], v[0:1]
	s_nop 0
	v_pk_mul_f32 v[0:1], v[0:1], s[36:37] op_sel_hi:[1,0]
	s_nop 0
	v_fma_f32 v1, -v0, v0, v1
	v_max_f32_e32 v1, 0, v1
	v_add_f32_e32 v1, 0x358637bd, v1
	v_mul_f32_e32 v19, 0x4b800000, v1
	v_cmp_gt_f32_e32 vcc, s89, v1
	v_sub_f32_e32 v8, v8, v0
	s_nop 0
	v_cndmask_b32_e32 v1, v1, v19, vcc
	v_rsq_f32_e32 v1, v1
	v_bfe_u32 v19, v18, 16, 1
	v_add3_u32 v18, v18, v19, s90
	ds_write_b16_d16_hi v17, v18 offset:448
	v_mul_f32_e32 v17, 0x45800000, v1
	v_cndmask_b32_e32 v1, v1, v17, vcc
	v_sub_f32_e32 v18, v24, v0
	v_mul_f32_e32 v18, v18, v1
	v_lshlrev_b32_e32 v17, 10, v211
	v_bfe_u32 v19, v18, 16, 1
	v_add3_u32 v18, v18, v19, s90
	v_add3_u32 v17, 0, v17, v16
	v_mul_f32_e32 v8, v8, v1
	ds_write_b16_d16_hi v17, v18
	v_bfe_u32 v18, v8, 16, 1
	v_add3_u32 v8, v8, v18, s90
	ds_write_b16_d16_hi v17, v8 offset:64
	v_sub_f32_e32 v8, v40, v0
	v_mul_f32_e32 v8, v8, v1
	v_bfe_u32 v18, v8, 16, 1
	v_add3_u32 v8, v8, v18, s90
	ds_write_b16_d16_hi v17, v8 offset:128
	v_sub_f32_e32 v8, v56, v0
	v_mul_f32_e32 v8, v8, v1
	v_bfe_u32 v18, v8, 16, 1
	v_add3_u32 v8, v8, v18, s90
	ds_write_b16_d16_hi v17, v8 offset:192
	v_sub_f32_e32 v8, v104, v0
	v_mul_f32_e32 v8, v8, v1
	v_bfe_u32 v18, v8, 16, 1
	v_add3_u32 v8, v8, v18, s90
	ds_write_b16_d16_hi v17, v8 offset:256
	v_sub_f32_e32 v8, v120, v0
	v_mul_f32_e32 v8, v8, v1
	v_bfe_u32 v18, v8, 16, 1
	v_add3_u32 v8, v8, v18, s90
	ds_write_b16_d16_hi v17, v8 offset:320
	v_sub_f32_e32 v8, v88, v0
	v_mul_f32_e32 v8, v8, v1
	v_bfe_u32 v18, v8, 16, 1
	v_add3_u32 v8, v8, v18, s90
	v_sub_f32_e32 v0, v72, v0
	ds_write_b16_d16_hi v17, v8 offset:384
	v_mul_f32_e32 v8, v0, v1
	v_pk_add_f32 v[0:1], v[142:143], v[2:3]
	s_nop 0
	v_pk_mul_f32 v[0:1], v[0:1], s[36:37] op_sel_hi:[1,0]
	s_nop 0
	v_fma_f32 v1, -v0, v0, v1
	v_max_f32_e32 v1, 0, v1
	v_add_f32_e32 v1, 0x358637bd, v1
	v_mul_f32_e32 v2, 0x4b800000, v1
	v_cmp_gt_f32_e32 vcc, s89, v1
	v_sub_f32_e32 v3, v25, v0
	s_nop 0
	v_cndmask_b32_e32 v1, v1, v2, vcc
	v_rsq_f32_e32 v1, v1
	v_bfe_u32 v2, v8, 16, 1
	v_add3_u32 v2, v8, v2, s90
	ds_write_b16_d16_hi v17, v2 offset:448
	v_mul_f32_e32 v2, 0x45800000, v1
	v_cndmask_b32_e32 v1, v1, v2, vcc
	v_mul_f32_e32 v3, v3, v1
	v_lshlrev_b32_e32 v2, 10, v210
	v_bfe_u32 v8, v3, 16, 1
	v_add3_u32 v3, v3, v8, s90
	v_add3_u32 v2, 0, v2, v16
	ds_write_b16_d16_hi v2, v3
	v_sub_f32_e32 v3, v9, v0
	v_mul_f32_e32 v3, v3, v1
	v_bfe_u32 v8, v3, 16, 1
	v_add3_u32 v3, v3, v8, s90
	ds_write_b16_d16_hi v2, v3 offset:64
	v_sub_f32_e32 v3, v41, v0
	v_mul_f32_e32 v3, v3, v1
	v_bfe_u32 v8, v3, 16, 1
	v_add3_u32 v3, v3, v8, s90
	ds_write_b16_d16_hi v2, v3 offset:128
	v_sub_f32_e32 v3, v57, v0
	v_mul_f32_e32 v3, v3, v1
	v_bfe_u32 v8, v3, 16, 1
	v_add3_u32 v3, v3, v8, s90
	ds_write_b16_d16_hi v2, v3 offset:192
	v_sub_f32_e32 v3, v105, v0
	v_mul_f32_e32 v3, v3, v1
	v_bfe_u32 v8, v3, 16, 1
	v_add3_u32 v3, v3, v8, s90
	ds_write_b16_d16_hi v2, v3 offset:256
	v_sub_f32_e32 v3, v121, v0
	v_mul_f32_e32 v3, v3, v1
	v_bfe_u32 v8, v3, 16, 1
	v_add3_u32 v3, v3, v8, s90
	ds_write_b16_d16_hi v2, v3 offset:320
	v_sub_f32_e32 v3, v89, v0
	v_mul_f32_e32 v3, v3, v1
	v_bfe_u32 v8, v3, 16, 1
	v_add3_u32 v3, v3, v8, s90
	v_sub_f32_e32 v0, v73, v0
	ds_write_b16_d16_hi v2, v3 offset:384
	v_mul_f32_e32 v3, v0, v1
	s_waitcnt lgkmcnt(14)
; #define LAS __attribute__((address_space(3)))
; __device__ __forceinline__ bf16_t f2bf(float f) { unsigned u = __builtin_bit_cast(unsigned, f); return (bf16_t)((u + 0x7fffu + ((u >> 16) & 1u)) >> 16); }
; __device__ __forceinline__ int crow(int r, int hi) { return (r & 3) + 8 * (r >> 2) + 4 * hi; }
; __device__ __forceinline__ int crow(int r, int hi) { return (r & 3) + 8 * (r >> 2) + 4 * hi; }
; template <int DK, int DV, bool MLSTM>
; __device__ __forceinline__ void out_unit2(LAS unsigned char* lds, LAS unsigned char* ldstab, const OutArgs a, const int wv) {
;     ...
;     for (int r = 0; r < 16; ++r) {
;         const int row = 32 * rb + crow(r, hi);
;         const float t1 = s1[r] + exch[((1 - dh) * 128 + row) * 2], t2 = s2[r] + exch[((1 - dh) * 128 + row) * 2 + 1];
;         float mean, inv;
;         if (MLSTM) { mean = 0.f; inv = rsqrtf(t2 * (1.f / DV) + EPS); }
;         else { mean = t1 * (1.f / DV); inv = rsqrtf(fmaxf(t2 * (1.f / DV) - mean * mean, 0.f) + EPS); }
; #pragma unroll
;         for (int nb = 0; nb < NB; ++nb) { const int col = dh * (DV / 2) + 32 * nb + r32;
;             *(LAS bf16_t*)(lds + row * TP + col * 2) = f2bf((o[nb][r] - mean) * inv); }
;     }
	v_pk_add_f32 v[0:1], v[136:137], v[4:5]
	s_nop 0
	v_pk_mul_f32 v[0:1], v[0:1], s[36:37] op_sel_hi:[1,0]
	s_nop 0
	v_fma_f32 v1, -v0, v0, v1
	v_max_f32_e32 v1, 0, v1
	v_add_f32_e32 v1, 0x358637bd, v1
	v_mul_f32_e32 v4, 0x4b800000, v1
	v_cmp_gt_f32_e32 vcc, s89, v1
	s_nop 1
	v_cndmask_b32_e32 v1, v1, v4, vcc
	v_rsq_f32_e32 v1, v1
	v_bfe_u32 v4, v3, 16, 1
	v_add3_u32 v3, v3, v4, s90
	ds_write_b16_d16_hi v2, v3 offset:448
	v_mul_f32_e32 v2, 0x45800000, v1
	v_cndmask_b32_e32 v1, v1, v2, vcc
	v_sub_f32_e32 v3, v26, v0
	v_mul_f32_e32 v3, v3, v1
	v_lshlrev_b32_e32 v2, 10, v209
	v_bfe_u32 v4, v3, 16, 1
	v_add3_u32 v3, v3, v4, s90
	v_add3_u32 v2, 0, v2, v16
	ds_write_b16_d16_hi v2, v3
	v_sub_f32_e32 v3, v10, v0
	v_mul_f32_e32 v3, v3, v1
	v_bfe_u32 v4, v3, 16, 1
	v_add3_u32 v3, v3, v4, s90
	ds_write_b16_d16_hi v2, v3 offset:64
	v_sub_f32_e32 v3, v42, v0
	v_mul_f32_e32 v3, v3, v1
	v_bfe_u32 v4, v3, 16, 1
	v_add3_u32 v3, v3, v4, s90
	ds_write_b16_d16_hi v2, v3 offset:128
	v_sub_f32_e32 v3, v58, v0
	v_mul_f32_e32 v3, v3, v1
	v_bfe_u32 v4, v3, 16, 1
	v_add3_u32 v3, v3, v4, s90
	ds_write_b16_d16_hi v2, v3 offset:192
	v_sub_f32_e32 v3, v106, v0
	v_mul_f32_e32 v3, v3, v1
	v_bfe_u32 v4, v3, 16, 1
	v_add3_u32 v3, v3, v4, s90
	ds_write_b16_d16_hi v2, v3 offset:256
	v_sub_f32_e32 v3, v122, v0
	v_mul_f32_e32 v3, v3, v1
	v_bfe_u32 v4, v3, 16, 1
	v_add3_u32 v3, v3, v4, s90
	ds_write_b16_d16_hi v2, v3 offset:320
	v_sub_f32_e32 v3, v90, v0
	v_mul_f32_e32 v3, v3, v1
	v_bfe_u32 v4, v3, 16, 1
	v_add3_u32 v3, v3, v4, s90
	v_sub_f32_e32 v0, v74, v0
	ds_write_b16_d16_hi v2, v3 offset:384
	v_mul_f32_e32 v3, v0, v1
	v_pk_add_f32 v[0:1], v[138:139], v[6:7]
	s_nop 0
	v_pk_mul_f32 v[0:1], v[0:1], s[36:37] op_sel_hi:[1,0]
	s_nop 0
	v_fma_f32 v1, -v0, v0, v1
	v_max_f32_e32 v1, 0, v1
	v_add_f32_e32 v1, 0x358637bd, v1
	v_mul_f32_e32 v4, 0x4b800000, v1
	v_cmp_gt_f32_e32 vcc, s89, v1
	s_nop 1
	v_cndmask_b32_e32 v1, v1, v4, vcc
	v_rsq_f32_e32 v1, v1
	v_bfe_u32 v4, v3, 16, 1
	v_add3_u32 v3, v3, v4, s90
	ds_write_b16_d16_hi v2, v3 offset:448
	v_mul_f32_e32 v2, 0x45800000, v1
	v_cndmask_b32_e32 v1, v1, v2, vcc
	v_sub_f32_e32 v3, v27, v0
	v_lshlrev_b32_e32 v2, 10, v208
	v_mul_f32_e32 v3, v3, v1
	v_bfe_u32 v4, v3, 16, 1
	v_add3_u32 v8, 0, v2, v16
	v_sub_f32_e32 v2, v11, v0
	v_add3_u32 v3, v3, v4, s90
	v_mul_f32_e32 v2, v2, v1
	ds_write_b16_d16_hi v8, v3
	v_bfe_u32 v3, v2, 16, 1
	v_add3_u32 v2, v2, v3, s90
	ds_write_b16_d16_hi v8, v2 offset:64
	v_sub_f32_e32 v2, v43, v0
	v_mul_f32_e32 v2, v2, v1
	v_bfe_u32 v3, v2, 16, 1
	v_add3_u32 v2, v2, v3, s90
	ds_write_b16_d16_hi v8, v2 offset:128
	v_sub_f32_e32 v2, v59, v0
	v_mul_f32_e32 v2, v2, v1
	v_bfe_u32 v3, v2, 16, 1
	v_add3_u32 v2, v2, v3, s90
	ds_write_b16_d16_hi v8, v2 offset:192
	v_sub_f32_e32 v2, v107, v0
	v_mul_f32_e32 v2, v2, v1
	v_bfe_u32 v3, v2, 16, 1
	v_add3_u32 v2, v2, v3, s90
	ds_write_b16_d16_hi v8, v2 offset:256
	v_sub_f32_e32 v2, v123, v0
	v_mul_f32_e32 v2, v2, v1
	v_bfe_u32 v3, v2, 16, 1
	v_add3_u32 v2, v2, v3, s90
	ds_write_b16_d16_hi v8, v2 offset:320
	v_sub_f32_e32 v2, v91, v0
	v_sub_f32_e32 v0, v75, v0
	v_mul_f32_e32 v2, v2, v1
	v_mul_f32_e32 v9, v0, v1
	v_lshlrev_b32_e32 v0, 1, v207
	v_bfe_u32 v3, v2, 16, 1
	v_subrev_u32_e32 v0, s6, v0
	v_add3_u32 v2, v2, v3, s90
	v_lshl_add_u32 v0, v0, 2, s4
	ds_write_b16_d16_hi v8, v2 offset:384
	ds_read2_b64 v[0:3], v0 offset0:128 offset1:129
	v_lshlrev_b32_e32 v4, 1, v162
	v_subrev_u32_e32 v4, s6, v4
	v_lshl_add_u32 v4, v4, 2, s4
	ds_read2_b64 v[4:7], v4 offset0:128 offset1:129
	s_waitcnt lgkmcnt(1)
	v_pk_add_f32 v[0:1], v[132:133], v[0:1]
	s_nop 0
	v_pk_mul_f32 v[0:1], v[0:1], s[36:37] op_sel_hi:[1,0]
	s_nop 0
	v_fma_f32 v1, -v0, v0, v1
	v_max_f32_e32 v1, 0, v1
	v_add_f32_e32 v1, 0x358637bd, v1
	v_mul_f32_e32 v10, 0x4b800000, v1
	v_cmp_gt_f32_e32 vcc, s89, v1
	s_nop 1
	v_cndmask_b32_e32 v1, v1, v10, vcc
	v_rsq_f32_e32 v1, v1
	v_bfe_u32 v10, v9, 16, 1
	v_add3_u32 v9, v9, v10, s90
	ds_write_b16_d16_hi v8, v9 offset:448
	v_mul_f32_e32 v8, 0x45800000, v1
	v_cndmask_b32_e32 v1, v1, v8, vcc
	v_sub_f32_e32 v9, v28, v0
	v_mul_f32_e32 v9, v9, v1
	v_lshlrev_b32_e32 v8, 10, v207
	v_bfe_u32 v10, v9, 16, 1
	v_add3_u32 v9, v9, v10, s90
	v_add3_u32 v8, 0, v8, v16
	ds_write_b16_d16_hi v8, v9
	v_sub_f32_e32 v9, v12, v0
	v_mul_f32_e32 v9, v9, v1
	v_bfe_u32 v10, v9, 16, 1
	v_add3_u32 v9, v9, v10, s90
	ds_write_b16_d16_hi v8, v9 offset:64
	v_sub_f32_e32 v9, v44, v0
	v_mul_f32_e32 v9, v9, v1
	v_bfe_u32 v10, v9, 16, 1
	v_add3_u32 v9, v9, v10, s90
	ds_write_b16_d16_hi v8, v9 offset:128
	v_sub_f32_e32 v9, v60, v0
	v_mul_f32_e32 v9, v9, v1
	v_bfe_u32 v10, v9, 16, 1
	v_add3_u32 v9, v9, v10, s90
	ds_write_b16_d16_hi v8, v9 offset:192
	v_sub_f32_e32 v9, v108, v0
	v_mul_f32_e32 v9, v9, v1
	v_bfe_u32 v10, v9, 16, 1
	v_add3_u32 v9, v9, v10, s90
	ds_write_b16_d16_hi v8, v9 offset:256
	v_sub_f32_e32 v9, v124, v0
	v_mul_f32_e32 v9, v9, v1
	v_bfe_u32 v10, v9, 16, 1
	v_add3_u32 v9, v9, v10, s90
	ds_write_b16_d16_hi v8, v9 offset:320
	v_sub_f32_e32 v9, v92, v0
	v_mul_f32_e32 v9, v9, v1
	v_bfe_u32 v10, v9, 16, 1
	v_add3_u32 v9, v9, v10, s90
	v_sub_f32_e32 v0, v76, v0
	ds_write_b16_d16_hi v8, v9 offset:384
	v_mul_f32_e32 v9, v0, v1
	v_pk_add_f32 v[0:1], v[134:135], v[2:3]
	s_nop 0
	v_pk_mul_f32 v[0:1], v[0:1], s[36:37] op_sel_hi:[1,0]
	s_nop 0
	v_fma_f32 v1, -v0, v0, v1
	v_max_f32_e32 v1, 0, v1
	v_add_f32_e32 v1, 0x358637bd, v1
	v_mul_f32_e32 v2, 0x4b800000, v1
	v_cmp_gt_f32_e32 vcc, s89, v1
	v_sub_f32_e32 v3, v29, v0
	s_nop 0
	v_cndmask_b32_e32 v1, v1, v2, vcc
	v_rsq_f32_e32 v1, v1
	v_bfe_u32 v2, v9, 16, 1
	v_add3_u32 v2, v9, v2, s90
	ds_write_b16_d16_hi v8, v2 offset:448
	v_mul_f32_e32 v2, 0x45800000, v1
	v_cndmask_b32_e32 v1, v1, v2, vcc
	v_mul_f32_e32 v3, v3, v1
	v_lshlrev_b32_e32 v2, 10, v206
	v_bfe_u32 v8, v3, 16, 1
	v_add3_u32 v3, v3, v8, s90
	v_add3_u32 v2, 0, v2, v16
	ds_write_b16_d16_hi v2, v3
	v_sub_f32_e32 v3, v13, v0
	v_mul_f32_e32 v3, v3, v1
	v_bfe_u32 v8, v3, 16, 1
	v_add3_u32 v3, v3, v8, s90
	ds_write_b16_d16_hi v2, v3 offset:64
	v_sub_f32_e32 v3, v45, v0
	v_mul_f32_e32 v3, v3, v1
	v_bfe_u32 v8, v3, 16, 1
	v_add3_u32 v3, v3, v8, s90
	ds_write_b16_d16_hi v2, v3 offset:128
	v_sub_f32_e32 v3, v61, v0
	v_mul_f32_e32 v3, v3, v1
	v_bfe_u32 v8, v3, 16, 1
	v_add3_u32 v3, v3, v8, s90
	ds_write_b16_d16_hi v2, v3 offset:192
	v_sub_f32_e32 v3, v109, v0
	v_mul_f32_e32 v3, v3, v1
	v_bfe_u32 v8, v3, 16, 1
	v_add3_u32 v3, v3, v8, s90
	ds_write_b16_d16_hi v2, v3 offset:256
	v_sub_f32_e32 v3, v125, v0
	v_mul_f32_e32 v3, v3, v1
	v_bfe_u32 v8, v3, 16, 1
	v_add3_u32 v3, v3, v8, s90
	ds_write_b16_d16_hi v2, v3 offset:320
	v_sub_f32_e32 v3, v93, v0
	v_mul_f32_e32 v3, v3, v1
	v_bfe_u32 v8, v3, 16, 1
	v_add3_u32 v3, v3, v8, s90
	v_sub_f32_e32 v0, v77, v0
	ds_write_b16_d16_hi v2, v3 offset:384
	v_mul_f32_e32 v3, v0, v1
	s_waitcnt lgkmcnt(14)
; #define LAS __attribute__((address_space(3)))
; __device__ __forceinline__ bf16_t f2bf(float f) { unsigned u = __builtin_bit_cast(unsigned, f); return (bf16_t)((u + 0x7fffu + ((u >> 16) & 1u)) >> 16); }
; template <int DK, int DV, bool MLSTM>
; __device__ __forceinline__ void out_unit2(LAS unsigned char* lds, LAS unsigned char* ldstab, const OutArgs a, const int wv) {
;     ...
;         for (int nb = 0; nb < NB; ++nb) { const int col = dh * (DV / 2) + 32 * nb + r32;
;             *(LAS bf16_t*)(lds + row * TP + col * 2) = f2bf((o[nb][r] - mean) * inv); }
;     }
;     __syncthreads();
;     constexpr int CPR = DV / 8;
; #pragma unroll 1
;     for (int id = tid; id < 128 * CPR; id += 512) { const int row = id / CPR, ch = id % CPR;
;         const u32x4 y = *(const LAS u32x4*)(lds + row * TP + ch * 16);
;         const f32x4 g0 = *(const f32x4*)(a.gain + 8 * ch), g1 = *(const f32x4*)(a.gain + 8 * ch + 4);
;         float yv[8] = {bf_lo(y.x), bf_hi(y.x), bf_lo(y.y), bf_hi(y.y), bf_lo(y.z), bf_hi(y.z), bf_lo(y.w), bf_hi(y.w)};
;         float gv[8];
;         if (MLSTM) { const u32x4 g = *(const u32x4*)(a.G + (size_t)row * a.ldg + 8 * ch);
;             gv[0] = bf_lo(g.x); gv[1] = bf_hi(g.x); gv[2] = bf_lo(g.y); gv[3] = bf_hi(g.y); gv[4] = bf_lo(g.z); gv[5] = bf_hi(g.z); gv[6] = bf_lo(g.w); gv[7] = bf_hi(g.w); }
;         else { const u32x2 g = *(const u32x2*)(a.G8 + (size_t)row * a.ldg8 + 8 * ch);
;             const f32x2 e0 = __builtin_amdgcn_cvt_pk_f32_fp8((int)g.x, false), e1 = __builtin_amdgcn_cvt_pk_f32_fp8((int)g.x, true), e2 = __builtin_amdgcn_cvt_pk_f32_fp8((int)g.y, false), e3 = __builtin_amdgcn_cvt_pk_f32_fp8((int)g.y, true);
;             gv[0] = e0[0] * a.g8inv; gv[1] = e0[1] * a.g8inv; gv[2] = e1[0] * a.g8inv; gv[3] = e1[1] * a.g8inv; gv[4] = e2[0] * a.g8inv; gv[5] = e2[1] * a.g8inv; gv[6] = e3[0] * a.g8inv; gv[7] = e3[1] * a.g8inv; }
;         float gn[8] = {g0[0], g0[1], g0[2], g0[3], g1[0], g1[1], g1[2], g1[3]};
;         float ov[8];
; #pragma unroll
;         for (int i = 0; i < 8; ++i) ov[i] = yv[i] * gn[i] * (MLSTM ? sigmoidf_(gv[i]) : siluf_(gv[i]));
;         u32x2 w; w.x = pg8::pk4_fp8c(ov[0] * a.oscale, ov[1] * a.oscale, ov[2] * a.oscale, ov[3] * a.oscale); w.y = pg8::pk4_fp8c(ov[4] * a.oscale, ov[5] * a.oscale, ov[6] * a.oscale, ov[7] * a.oscale);
;         *(u32x2*)(a.Out + (size_t)row * a.ldo + 8 * ch) = w; }
	v_pk_add_f32 v[0:1], v[128:129], v[4:5]
	s_nop 0
	v_pk_mul_f32 v[0:1], v[0:1], s[36:37] op_sel_hi:[1,0]
	s_nop 0
	v_fma_f32 v1, -v0, v0, v1
	v_max_f32_e32 v1, 0, v1
	v_add_f32_e32 v1, 0x358637bd, v1
	v_mul_f32_e32 v4, 0x4b800000, v1
	v_cmp_gt_f32_e32 vcc, s89, v1
	s_nop 1
	v_cndmask_b32_e32 v1, v1, v4, vcc
	v_rsq_f32_e32 v1, v1
	v_bfe_u32 v4, v3, 16, 1
	v_add3_u32 v3, v3, v4, s90
	ds_write_b16_d16_hi v2, v3 offset:448
	v_mul_f32_e32 v2, 0x45800000, v1
	v_cndmask_b32_e32 v1, v1, v2, vcc
	v_sub_f32_e32 v3, v30, v0
	v_mul_f32_e32 v3, v3, v1
	v_lshlrev_b32_e32 v2, 10, v162
	v_bfe_u32 v4, v3, 16, 1
	v_add3_u32 v3, v3, v4, s90
	v_add3_u32 v2, 0, v2, v16
	ds_write_b16_d16_hi v2, v3
	v_sub_f32_e32 v3, v14, v0
	v_mul_f32_e32 v3, v3, v1
	v_bfe_u32 v4, v3, 16, 1
	v_add3_u32 v3, v3, v4, s90
	ds_write_b16_d16_hi v2, v3 offset:64
	v_sub_f32_e32 v3, v46, v0
	v_mul_f32_e32 v3, v3, v1
	v_bfe_u32 v4, v3, 16, 1
	v_add3_u32 v3, v3, v4, s90
	ds_write_b16_d16_hi v2, v3 offset:128
	v_sub_f32_e32 v3, v62, v0
	v_mul_f32_e32 v3, v3, v1
	v_bfe_u32 v4, v3, 16, 1
	v_add3_u32 v3, v3, v4, s90
	ds_write_b16_d16_hi v2, v3 offset:192
	v_sub_f32_e32 v3, v110, v0
	v_mul_f32_e32 v3, v3, v1
	v_bfe_u32 v4, v3, 16, 1
	v_add3_u32 v3, v3, v4, s90
	ds_write_b16_d16_hi v2, v3 offset:256
	v_sub_f32_e32 v3, v126, v0
	v_mul_f32_e32 v3, v3, v1
	v_bfe_u32 v4, v3, 16, 1
	v_add3_u32 v3, v3, v4, s90
	ds_write_b16_d16_hi v2, v3 offset:320
	v_sub_f32_e32 v3, v94, v0
	v_mul_f32_e32 v3, v3, v1
	v_bfe_u32 v4, v3, 16, 1
	v_add3_u32 v3, v3, v4, s90
	v_sub_f32_e32 v0, v78, v0
	ds_write_b16_d16_hi v2, v3 offset:384
	v_mul_f32_e32 v3, v0, v1
	v_pk_add_f32 v[0:1], v[130:131], v[6:7]
	s_nop 0
	v_pk_mul_f32 v[0:1], v[0:1], s[36:37] op_sel_hi:[1,0]
	s_nop 0
	v_fma_f32 v1, -v0, v0, v1
	v_max_f32_e32 v1, 0, v1
	v_add_f32_e32 v1, 0x358637bd, v1
	v_mul_f32_e32 v4, 0x4b800000, v1
	v_cmp_gt_f32_e32 vcc, s89, v1
	s_nop 1
	v_cndmask_b32_e32 v1, v1, v4, vcc
	v_rsq_f32_e32 v1, v1
	v_bfe_u32 v4, v3, 16, 1
	v_add3_u32 v3, v3, v4, s90
	ds_write_b16_d16_hi v2, v3 offset:448
	v_mul_f32_e32 v2, 0x45800000, v1
	v_cndmask_b32_e32 v1, v1, v2, vcc
	v_sub_f32_e32 v3, v31, v0
	v_mul_f32_e32 v3, v3, v1
	v_lshlrev_b32_e32 v2, 10, v160
	v_bfe_u32 v4, v3, 16, 1
	v_add3_u32 v3, v3, v4, s90
	v_add3_u32 v2, 0, v2, v16
	ds_write_b16_d16_hi v2, v3
	v_sub_f32_e32 v3, v15, v0
	v_mul_f32_e32 v3, v3, v1
	v_bfe_u32 v4, v3, 16, 1
	v_add3_u32 v3, v3, v4, s90
	ds_write_b16_d16_hi v2, v3 offset:64
	v_sub_f32_e32 v3, v47, v0
	v_mul_f32_e32 v3, v3, v1
	v_bfe_u32 v4, v3, 16, 1
	v_add3_u32 v3, v3, v4, s90
	ds_write_b16_d16_hi v2, v3 offset:128
	v_sub_f32_e32 v3, v63, v0
	v_mul_f32_e32 v3, v3, v1
	v_bfe_u32 v4, v3, 16, 1
	v_add3_u32 v3, v3, v4, s90
	ds_write_b16_d16_hi v2, v3 offset:192
	v_sub_f32_e32 v3, v111, v0
	v_mul_f32_e32 v3, v3, v1
	v_bfe_u32 v4, v3, 16, 1
	v_add3_u32 v3, v3, v4, s90
	ds_write_b16_d16_hi v2, v3 offset:256
	v_sub_f32_e32 v3, v127, v0
	v_mul_f32_e32 v3, v3, v1
	v_bfe_u32 v4, v3, 16, 1
	v_add3_u32 v3, v3, v4, s90
	ds_write_b16_d16_hi v2, v3 offset:320
	v_sub_f32_e32 v3, v95, v0
	v_sub_f32_e32 v0, v79, v0
	v_mul_f32_e32 v3, v3, v1
	v_mul_f32_e32 v0, v0, v1
	v_bfe_u32 v4, v3, 16, 1
	v_bfe_u32 v1, v0, 16, 1
	v_add3_u32 v3, v3, v4, s90
	v_add3_u32 v0, v0, v1, s90
	v_cmp_gt_i32_e32 vcc, s88, v232
	ds_write_b16_d16_hi v2, v3 offset:384
	ds_write_b16_d16_hi v2, v0 offset:448
	s_waitcnt lgkmcnt(0)
	s_barrier
	s_and_saveexec_b64 s[38:39], vcc
	s_cbranch_execz .LBB0_1826
	s_lshl_b32 s4, s8, 2
	s_add_u32 s40, s24, s4
	s_addc_u32 s41, s25, 0
	s_lshl_b64 s[2:3], s[2:3], 11
	s_add_u32 s4, s53, s2
	s_addc_u32 s5, s54, s3
	s_add_u32 s42, s4, s8
	s_addc_u32 s43, s5, 0
	s_add_u32 s2, s55, s2
	s_addc_u32 s3, s56, s3
	s_add_u32 s44, s2, s8
	s_addc_u32 s45, s3, 0
	v_lshl_add_u32 v4, v232, 4, 0
	v_lshlrev_b32_e32 v5, 3, v232
	s_mov_b64 s[46:47], 0
	v_and_b32_e32 v6, 63, v232
	v_lshrrev_b32_e32 v7, 6, v232
	v_lshlrev_b32_e32 v8, 5, v6
	v_lshlrev_b32_e32 v5, 3, v6
	v_lshl_add_u32 v5, v7, 11, v5
	ds_read_b128 v[0:3], v4
	v_add_u32_e32 v4, 0x2000, v4
	global_load_dwordx4 v[40:43], v8, s[40:41]
	global_load_dwordx4 v[44:47], v8, s[40:41] offset:16
	global_load_dwordx2 v[30:31], v5, s[42:43]
	v_add_u32_e32 v23, 0x4000, v5
	s_nop 0
	global_load_dwordx2 v[6:7], v23, s[42:43]
	v_add_u32_e32 v23, 0x4000, v23
	v_mov_b32_e32 v162, v163
	s_mov_b32 s98, 0xbfb8aa3b
	s_mov_b32 s100, 0x41800000
	s_movk_i32 s46, 8
	s_waitcnt vmcnt(1)
.Ldloop0:
	s_waitcnt vmcnt(2) lgkmcnt(0)
	v_lshlrev_b32_e32 v10, 16, v0
	v_and_b32_e32 v11, 0xffff0000, v0
	v_lshlrev_b32_e32 v12, 16, v1
	v_and_b32_e32 v13, 0xffff0000, v1
	v_lshlrev_b32_e32 v14, 16, v2
	v_and_b32_e32 v15, 0xffff0000, v2
	v_lshlrev_b32_e32 v16, 16, v3
	v_and_b32_e32 v17, 0xffff0000, v3
	v_cvt_pk_f32_fp8_e32 v[32:33], v30
	v_cvt_pk_f32_fp8_sdwa v[34:35], v30 src0_sel:WORD_1
	v_cvt_pk_f32_fp8_e32 v[36:37], v31
	v_cvt_pk_f32_fp8_sdwa v[38:39], v31 src0_sel:WORD_1
	ds_read_b128 v[0:3], v4
	v_add_u32_e32 v4, 0x2000, v4
	s_cmp_eq_u32 s46, 1
	s_cbranch_scc1 .Ldloop0a
	global_load_dwordx2 v[30:31], v23, s[42:43]
	v_add_u32_e32 v23, 0x4000, v23
; #define LAS __attribute__((address_space(3)))
; __device__ __forceinline__ float sigmoidf_(float x) { return 1.f / (1.f + __expf(-x)); }
; __device__ __forceinline__ float siluf_(float x) { return x / (1.f + __expf(-x)); }
; __device__ __forceinline__ unsigned pk4_fp8c(float a, float b, float c, float d) { return pk4_fp8(__builtin_amdgcn_fmed3f(a, -448.f, 448.f), __builtin_amdgcn_fmed3f(b, -448.f, 448.f), __builtin_amdgcn_fmed3f(c, -448.f, 448.f), __builtin_amdgcn_fmed3f(d, -448.f, 448.f)); }
; template <int DK, int DV, bool MLSTM>
; __device__ __forceinline__ void out_unit2(LAS unsigned char* lds, LAS unsigned char* ldstab, const OutArgs a, const int wv) {
;     ...
;     for (int id = tid; id < 128 * CPR; id += 512) { const int row = id / CPR, ch = id % CPR;
;         const u32x4 y = *(const LAS u32x4*)(lds + row * TP + ch * 16);
;         const f32x4 g0 = *(const f32x4*)(a.gain + 8 * ch), g1 = *(const f32x4*)(a.gain + 8 * ch + 4);
;         float yv[8] = {bf_lo(y.x), bf_hi(y.x), bf_lo(y.y), bf_hi(y.y), bf_lo(y.z), bf_hi(y.z), bf_lo(y.w), bf_hi(y.w)};
;         float gv[8];
;         if (MLSTM) { const u32x4 g = *(const u32x4*)(a.G + (size_t)row * a.ldg + 8 * ch);
;             gv[0] = bf_lo(g.x); gv[1] = bf_hi(g.x); gv[2] = bf_lo(g.y); gv[3] = bf_hi(g.y); gv[4] = bf_lo(g.z); gv[5] = bf_hi(g.z); gv[6] = bf_lo(g.w); gv[7] = bf_hi(g.w); }
;         else { const u32x2 g = *(const u32x2*)(a.G8 + (size_t)row * a.ldg8 + 8 * ch);
;             const f32x2 e0 = __builtin_amdgcn_cvt_pk_f32_fp8((int)g.x, false), e1 = __builtin_amdgcn_cvt_pk_f32_fp8((int)g.x, true), e2 = __builtin_amdgcn_cvt_pk_f32_fp8((int)g.y, false), e3 = __builtin_amdgcn_cvt_pk_f32_fp8((int)g.y, true);
;             gv[0] = e0[0] * a.g8inv; gv[1] = e0[1] * a.g8inv; gv[2] = e1[0] * a.g8inv; gv[3] = e1[1] * a.g8inv; gv[4] = e2[0] * a.g8inv; gv[5] = e2[1] * a.g8inv; gv[6] = e3[0] * a.g8inv; gv[7] = e3[1] * a.g8inv; }
;         float gn[8] = {g0[0], g0[1], g0[2], g0[3], g1[0], g1[1], g1[2], g1[3]};
;         float ov[8];
; #pragma unroll
;         for (int i = 0; i < 8; ++i) ov[i] = yv[i] * gn[i] * (MLSTM ? sigmoidf_(gv[i]) : siluf_(gv[i]));
;         u32x2 w; w.x = pg8::pk4_fp8c(ov[0] * a.oscale, ov[1] * a.oscale, ov[2] * a.oscale, ov[3] * a.oscale); w.y = pg8::pk4_fp8c(ov[4] * a.oscale, ov[5] * a.oscale, ov[6] * a.oscale, ov[7] * a.oscale);
;         *(u32x2*)(a.Out + (size_t)row * a.ldo + 8 * ch) = w; }
.Ldloop0a:
	v_pk_mul_f32 v[10:11], v[40:41], v[10:11]
	v_pk_mul_f32 v[12:13], v[42:43], v[12:13]
	v_pk_mul_f32 v[14:15], v[44:45], v[14:15]
	v_pk_mul_f32 v[16:17], v[46:47], v[16:17]
	v_pk_mul_f32 v[32:33], v[32:33], v[162:163]
	v_pk_mul_f32 v[34:35], v[34:35], v[162:163]
	v_pk_mul_f32 v[36:37], v[36:37], v[162:163]
	v_pk_mul_f32 v[38:39], v[38:39], v[162:163]
	v_pk_mul_f32 v[48:49], v[32:33], s[98:99] op_sel_hi:[1,0]
	v_pk_mul_f32 v[50:51], v[34:35], s[98:99] op_sel_hi:[1,0]
	v_pk_mul_f32 v[52:53], v[36:37], s[98:99] op_sel_hi:[1,0]
	v_pk_mul_f32 v[54:55], v[38:39], s[98:99] op_sel_hi:[1,0]
	v_exp_f32_e32 v48, v48
	v_exp_f32_e32 v49, v49
	v_exp_f32_e32 v50, v50
	v_exp_f32_e32 v51, v51
	v_exp_f32_e32 v52, v52
	v_exp_f32_e32 v53, v53
	v_exp_f32_e32 v54, v54
	v_exp_f32_e32 v55, v55
	v_pk_add_f32 v[48:49], v[48:49], 1.0 op_sel_hi:[1,0]
	v_pk_add_f32 v[50:51], v[50:51], 1.0 op_sel_hi:[1,0]
	v_pk_add_f32 v[52:53], v[52:53], 1.0 op_sel_hi:[1,0]
	v_pk_add_f32 v[54:55], v[54:55], 1.0 op_sel_hi:[1,0]
	v_rcp_f32_e32 v56, v48
	v_rcp_f32_e32 v57, v49
	v_rcp_f32_e32 v58, v50
	v_rcp_f32_e32 v59, v51
	v_rcp_f32_e32 v60, v52
	v_rcp_f32_e32 v61, v53
	v_rcp_f32_e32 v62, v54
	v_rcp_f32_e32 v63, v55
	v_pk_fma_f32 v[8:9], v[48:49], v[56:57], 1.0 op_sel_hi:[1,1,0] neg_lo:[1,0,0] neg_hi:[1,0,0]
	v_pk_fma_f32 v[18:19], v[50:51], v[58:59], 1.0 op_sel_hi:[1,1,0] neg_lo:[1,0,0] neg_hi:[1,0,0]
	v_pk_fma_f32 v[20:21], v[52:53], v[60:61], 1.0 op_sel_hi:[1,1,0] neg_lo:[1,0,0] neg_hi:[1,0,0]
	v_pk_fma_f32 v[26:27], v[54:55], v[62:63], 1.0 op_sel_hi:[1,1,0] neg_lo:[1,0,0] neg_hi:[1,0,0]
	v_pk_fma_f32 v[56:57], v[8:9], v[56:57], v[56:57]
	v_pk_fma_f32 v[58:59], v[18:19], v[58:59], v[58:59]
	v_pk_fma_f32 v[60:61], v[20:21], v[60:61], v[60:61]
	v_pk_fma_f32 v[62:63], v[26:27], v[62:63], v[62:63]
	v_pk_mul_f32 v[64:65], v[32:33], v[56:57]
	v_pk_mul_f32 v[66:67], v[34:35], v[58:59]
	v_pk_mul_f32 v[68:69], v[36:37], v[60:61]
	v_pk_mul_f32 v[70:71], v[38:39], v[62:63]
	v_pk_fma_f32 v[8:9], v[48:49], v[64:65], v[32:33] neg_lo:[1,0,0] neg_hi:[1,0,0]
	v_pk_fma_f32 v[18:19], v[50:51], v[66:67], v[34:35] neg_lo:[1,0,0] neg_hi:[1,0,0]
	v_pk_fma_f32 v[20:21], v[52:53], v[68:69], v[36:37] neg_lo:[1,0,0] neg_hi:[1,0,0]
	v_pk_fma_f32 v[26:27], v[54:55], v[70:71], v[38:39] neg_lo:[1,0,0] neg_hi:[1,0,0]
	v_pk_fma_f32 v[64:65], v[8:9], v[56:57], v[64:65]
	v_pk_fma_f32 v[66:67], v[18:19], v[58:59], v[66:67]
	v_pk_fma_f32 v[68:69], v[20:21], v[60:61], v[68:69]
	v_pk_fma_f32 v[70:71], v[26:27], v[62:63], v[70:71]
	v_pk_fma_f32 v[8:9], v[48:49], v[64:65], v[32:33] neg_lo:[1,0,0] neg_hi:[1,0,0]
	v_pk_fma_f32 v[18:19], v[50:51], v[66:67], v[34:35] neg_lo:[1,0,0] neg_hi:[1,0,0]
	v_pk_fma_f32 v[20:21], v[52:53], v[68:69], v[36:37] neg_lo:[1,0,0] neg_hi:[1,0,0]
	v_pk_fma_f32 v[26:27], v[54:55], v[70:71], v[38:39] neg_lo:[1,0,0] neg_hi:[1,0,0]
	v_pk_fma_f32 v[8:9], v[8:9], v[56:57], v[64:65]
	v_pk_fma_f32 v[18:19], v[18:19], v[58:59], v[66:67]
	v_pk_fma_f32 v[20:21], v[20:21], v[60:61], v[68:69]
	v_pk_fma_f32 v[26:27], v[26:27], v[62:63], v[70:71]
	v_div_fixup_f32 v8, v8, v48, v32
	v_div_fixup_f32 v9, v9, v49, v33
	v_div_fixup_f32 v18, v18, v50, v34
	v_div_fixup_f32 v19, v19, v51, v35
	v_div_fixup_f32 v20, v20, v52, v36
	v_div_fixup_f32 v21, v21, v53, v37
	v_div_fixup_f32 v26, v26, v54, v38
	v_div_fixup_f32 v27, v27, v55, v39
	v_pk_mul_f32 v[10:11], v[10:11], v[8:9]
	v_pk_mul_f32 v[12:13], v[12:13], v[18:19]
	v_pk_mul_f32 v[14:15], v[14:15], v[20:21]
	v_pk_mul_f32 v[16:17], v[16:17], v[26:27]
	v_pk_mul_f32 v[10:11], v[10:11], s[100:101] op_sel_hi:[1,0]
	v_pk_mul_f32 v[12:13], v[12:13], s[100:101] op_sel_hi:[1,0]
	v_pk_mul_f32 v[14:15], v[14:15], s[100:101] op_sel_hi:[1,0]
	v_pk_mul_f32 v[16:17], v[16:17], s[100:101] op_sel_hi:[1,0]
	v_med3_f32 v10, v10, s91, v231
	v_med3_f32 v11, v11, s91, v231
	v_med3_f32 v12, v12, s91, v231
	v_med3_f32 v13, v13, s91, v231
	v_med3_f32 v14, v14, s91, v231
	v_med3_f32 v15, v15, s91, v231
	v_med3_f32 v16, v16, s91, v231
	v_med3_f32 v17, v17, s91, v231
	v_cvt_pk_fp8_f32 v24, v10, v11
	v_cvt_pk_fp8_f32 v25, v14, v15
	s_nop 0
	v_cvt_pk_fp8_f32 v24, v12, v13 op_sel:[0,0,1]
	v_cvt_pk_fp8_f32 v25, v16, v17 op_sel:[0,0,1]
	s_nop 0
	global_store_dwordx2 v5, v[24:25], s[44:45]
	v_add_u32_e32 v5, 0x4000, v5
	s_waitcnt vmcnt(2) lgkmcnt(0)
	v_lshlrev_b32_e32 v10, 16, v0
	v_and_b32_e32 v11, 0xffff0000, v0
	v_lshlrev_b32_e32 v12, 16, v1
	v_and_b32_e32 v13, 0xffff0000, v1
	v_lshlrev_b32_e32 v14, 16, v2
	v_and_b32_e32 v15, 0xffff0000, v2
	v_lshlrev_b32_e32 v16, 16, v3
	v_and_b32_e32 v17, 0xffff0000, v3
	v_cvt_pk_f32_fp8_e32 v[32:33], v6
	v_cvt_pk_f32_fp8_sdwa v[34:35], v6 src0_sel:WORD_1
	v_cvt_pk_f32_fp8_e32 v[36:37], v7
	v_cvt_pk_f32_fp8_sdwa v[38:39], v7 src0_sel:WORD_1
	ds_read_b128 v[0:3], v4
	v_add_u32_e32 v4, 0x2000, v4
	s_cmp_eq_u32 s46, 1
	s_cbranch_scc1 .Ldloop0b
	global_load_dwordx2 v[6:7], v23, s[42:43]
	v_add_u32_e32 v23, 0x4000, v23
; #define LAS __attribute__((address_space(3)))
; __device__ __forceinline__ float sigmoidf_(float x) { return 1.f / (1.f + __expf(-x)); }
; __device__ __forceinline__ float siluf_(float x) { return x / (1.f + __expf(-x)); }
; __device__ __forceinline__ unsigned pk4_fp8c(float a, float b, float c, float d) { return pk4_fp8(__builtin_amdgcn_fmed3f(a, -448.f, 448.f), __builtin_amdgcn_fmed3f(b, -448.f, 448.f), __builtin_amdgcn_fmed3f(c, -448.f, 448.f), __builtin_amdgcn_fmed3f(d, -448.f, 448.f)); }
; template <int DK, int DV, bool MLSTM>
; __device__ __forceinline__ void out_unit2(LAS unsigned char* lds, LAS unsigned char* ldstab, const OutArgs a, const int wv) {
;     ...
;     for (int id = tid; id < 128 * CPR; id += 512) { const int row = id / CPR, ch = id % CPR;
;         const u32x4 y = *(const LAS u32x4*)(lds + row * TP + ch * 16);
;         const f32x4 g0 = *(const f32x4*)(a.gain + 8 * ch), g1 = *(const f32x4*)(a.gain + 8 * ch + 4);
;         float yv[8] = {bf_lo(y.x), bf_hi(y.x), bf_lo(y.y), bf_hi(y.y), bf_lo(y.z), bf_hi(y.z), bf_lo(y.w), bf_hi(y.w)};
;         float gv[8];
;         if (MLSTM) { const u32x4 g = *(const u32x4*)(a.G + (size_t)row * a.ldg + 8 * ch);
;             gv[0] = bf_lo(g.x); gv[1] = bf_hi(g.x); gv[2] = bf_lo(g.y); gv[3] = bf_hi(g.y); gv[4] = bf_lo(g.z); gv[5] = bf_hi(g.z); gv[6] = bf_lo(g.w); gv[7] = bf_hi(g.w); }
;         else { const u32x2 g = *(const u32x2*)(a.G8 + (size_t)row * a.ldg8 + 8 * ch);
;             const f32x2 e0 = __builtin_amdgcn_cvt_pk_f32_fp8((int)g.x, false), e1 = __builtin_amdgcn_cvt_pk_f32_fp8((int)g.x, true), e2 = __builtin_amdgcn_cvt_pk_f32_fp8((int)g.y, false), e3 = __builtin_amdgcn_cvt_pk_f32_fp8((int)g.y, true);
;             gv[0] = e0[0] * a.g8inv; gv[1] = e0[1] * a.g8inv; gv[2] = e1[0] * a.g8inv; gv[3] = e1[1] * a.g8inv; gv[4] = e2[0] * a.g8inv; gv[5] = e2[1] * a.g8inv; gv[6] = e3[0] * a.g8inv; gv[7] = e3[1] * a.g8inv; }
;         float gn[8] = {g0[0], g0[1], g0[2], g0[3], g1[0], g1[1], g1[2], g1[3]};
;         float ov[8];
; #pragma unroll
;         for (int i = 0; i < 8; ++i) ov[i] = yv[i] * gn[i] * (MLSTM ? sigmoidf_(gv[i]) : siluf_(gv[i]));
;         u32x2 w; w.x = pg8::pk4_fp8c(ov[0] * a.oscale, ov[1] * a.oscale, ov[2] * a.oscale, ov[3] * a.oscale); w.y = pg8::pk4_fp8c(ov[4] * a.oscale, ov[5] * a.oscale, ov[6] * a.oscale, ov[7] * a.oscale);
;         *(u32x2*)(a.Out + (size_t)row * a.ldo + 8 * ch) = w; }
.Ldloop0b:
	v_pk_mul_f32 v[10:11], v[40:41], v[10:11]
	v_pk_mul_f32 v[12:13], v[42:43], v[12:13]
	v_pk_mul_f32 v[14:15], v[44:45], v[14:15]
	v_pk_mul_f32 v[16:17], v[46:47], v[16:17]
	v_pk_mul_f32 v[32:33], v[32:33], v[162:163]
	v_pk_mul_f32 v[34:35], v[34:35], v[162:163]
	v_pk_mul_f32 v[36:37], v[36:37], v[162:163]
	v_pk_mul_f32 v[38:39], v[38:39], v[162:163]
	v_pk_mul_f32 v[48:49], v[32:33], s[98:99] op_sel_hi:[1,0]
	v_pk_mul_f32 v[50:51], v[34:35], s[98:99] op_sel_hi:[1,0]
	v_pk_mul_f32 v[52:53], v[36:37], s[98:99] op_sel_hi:[1,0]
	v_pk_mul_f32 v[54:55], v[38:39], s[98:99] op_sel_hi:[1,0]
	v_exp_f32_e32 v48, v48
	v_exp_f32_e32 v49, v49
	v_exp_f32_e32 v50, v50
	v_exp_f32_e32 v51, v51
	v_exp_f32_e32 v52, v52
	v_exp_f32_e32 v53, v53
	v_exp_f32_e32 v54, v54
	v_exp_f32_e32 v55, v55
	v_pk_add_f32 v[48:49], v[48:49], 1.0 op_sel_hi:[1,0]
	v_pk_add_f32 v[50:51], v[50:51], 1.0 op_sel_hi:[1,0]
	v_pk_add_f32 v[52:53], v[52:53], 1.0 op_sel_hi:[1,0]
	v_pk_add_f32 v[54:55], v[54:55], 1.0 op_sel_hi:[1,0]
	v_rcp_f32_e32 v56, v48
	v_rcp_f32_e32 v57, v49
	v_rcp_f32_e32 v58, v50
	v_rcp_f32_e32 v59, v51
	v_rcp_f32_e32 v60, v52
	v_rcp_f32_e32 v61, v53
	v_rcp_f32_e32 v62, v54
	v_rcp_f32_e32 v63, v55
	v_pk_fma_f32 v[8:9], v[48:49], v[56:57], 1.0 op_sel_hi:[1,1,0] neg_lo:[1,0,0] neg_hi:[1,0,0]
	v_pk_fma_f32 v[18:19], v[50:51], v[58:59], 1.0 op_sel_hi:[1,1,0] neg_lo:[1,0,0] neg_hi:[1,0,0]
	v_pk_fma_f32 v[20:21], v[52:53], v[60:61], 1.0 op_sel_hi:[1,1,0] neg_lo:[1,0,0] neg_hi:[1,0,0]
	v_pk_fma_f32 v[26:27], v[54:55], v[62:63], 1.0 op_sel_hi:[1,1,0] neg_lo:[1,0,0] neg_hi:[1,0,0]
	v_pk_fma_f32 v[56:57], v[8:9], v[56:57], v[56:57]
	v_pk_fma_f32 v[58:59], v[18:19], v[58:59], v[58:59]
	v_pk_fma_f32 v[60:61], v[20:21], v[60:61], v[60:61]
	v_pk_fma_f32 v[62:63], v[26:27], v[62:63], v[62:63]
	v_pk_mul_f32 v[64:65], v[32:33], v[56:57]
	v_pk_mul_f32 v[66:67], v[34:35], v[58:59]
	v_pk_mul_f32 v[68:69], v[36:37], v[60:61]
	v_pk_mul_f32 v[70:71], v[38:39], v[62:63]
	v_pk_fma_f32 v[8:9], v[48:49], v[64:65], v[32:33] neg_lo:[1,0,0] neg_hi:[1,0,0]
	v_pk_fma_f32 v[18:19], v[50:51], v[66:67], v[34:35] neg_lo:[1,0,0] neg_hi:[1,0,0]
	v_pk_fma_f32 v[20:21], v[52:53], v[68:69], v[36:37] neg_lo:[1,0,0] neg_hi:[1,0,0]
	v_pk_fma_f32 v[26:27], v[54:55], v[70:71], v[38:39] neg_lo:[1,0,0] neg_hi:[1,0,0]
	v_pk_fma_f32 v[64:65], v[8:9], v[56:57], v[64:65]
	v_pk_fma_f32 v[66:67], v[18:19], v[58:59], v[66:67]
	v_pk_fma_f32 v[68:69], v[20:21], v[60:61], v[68:69]
	v_pk_fma_f32 v[70:71], v[26:27], v[62:63], v[70:71]
	v_pk_fma_f32 v[8:9], v[48:49], v[64:65], v[32:33] neg_lo:[1,0,0] neg_hi:[1,0,0]
	v_pk_fma_f32 v[18:19], v[50:51], v[66:67], v[34:35] neg_lo:[1,0,0] neg_hi:[1,0,0]
	v_pk_fma_f32 v[20:21], v[52:53], v[68:69], v[36:37] neg_lo:[1,0,0] neg_hi:[1,0,0]
	v_pk_fma_f32 v[26:27], v[54:55], v[70:71], v[38:39] neg_lo:[1,0,0] neg_hi:[1,0,0]
	v_pk_fma_f32 v[8:9], v[8:9], v[56:57], v[64:65]
	v_pk_fma_f32 v[18:19], v[18:19], v[58:59], v[66:67]
	v_pk_fma_f32 v[20:21], v[20:21], v[60:61], v[68:69]
	v_pk_fma_f32 v[26:27], v[26:27], v[62:63], v[70:71]
	v_div_fixup_f32 v8, v8, v48, v32
	v_div_fixup_f32 v9, v9, v49, v33
	v_div_fixup_f32 v18, v18, v50, v34
	v_div_fixup_f32 v19, v19, v51, v35
	v_div_fixup_f32 v20, v20, v52, v36
	v_div_fixup_f32 v21, v21, v53, v37
	v_div_fixup_f32 v26, v26, v54, v38
	v_div_fixup_f32 v27, v27, v55, v39
	v_pk_mul_f32 v[10:11], v[10:11], v[8:9]
	v_pk_mul_f32 v[12:13], v[12:13], v[18:19]
	v_pk_mul_f32 v[14:15], v[14:15], v[20:21]
	v_pk_mul_f32 v[16:17], v[16:17], v[26:27]
	v_pk_mul_f32 v[10:11], v[10:11], s[100:101] op_sel_hi:[1,0]
	v_pk_mul_f32 v[12:13], v[12:13], s[100:101] op_sel_hi:[1,0]
	v_pk_mul_f32 v[14:15], v[14:15], s[100:101] op_sel_hi:[1,0]
	v_pk_mul_f32 v[16:17], v[16:17], s[100:101] op_sel_hi:[1,0]
	v_med3_f32 v10, v10, s91, v231
	v_med3_f32 v11, v11, s91, v231
	v_med3_f32 v12, v12, s91, v231
	v_med3_f32 v13, v13, s91, v231
	v_med3_f32 v14, v14, s91, v231
	v_med3_f32 v15, v15, s91, v231
	v_med3_f32 v16, v16, s91, v231
	v_med3_f32 v17, v17, s91, v231
	v_cvt_pk_fp8_f32 v24, v10, v11
	v_cvt_pk_fp8_f32 v25, v14, v15
	s_nop 0
	v_cvt_pk_fp8_f32 v24, v12, v13 op_sel:[0,0,1]
	v_cvt_pk_fp8_f32 v25, v16, v17 op_sel:[0,0,1]
	s_nop 0
	global_store_dwordx2 v5, v[24:25], s[44:45]
	v_add_u32_e32 v5, 0x4000, v5
	s_add_i32 s46, s46, -1
	s_cmp_lg_u32 s46, 0
	s_cbranch_scc1 .Ldloop0
	s_waitcnt lgkmcnt(0)
	s_branch .LBB0_1826

; #define LAS __attribute__((address_space(3)))
; __device__ __forceinline__ bf16_t f2bf(float f) { unsigned u = __builtin_bit_cast(unsigned, f); return (bf16_t)((u + 0x7fffu + ((u >> 16) & 1u)) >> 16); }
; __device__ __forceinline__ int crow(int r, int hi) { return (r & 3) + 8 * (r >> 2) + 4 * hi; }
; __device__ __forceinline__ int crow(int r, int hi) { return (r & 3) + 8 * (r >> 2) + 4 * hi; }
; template <int DK, int DV, bool MLSTM>
; __device__ __forceinline__ void out_unit2(LAS unsigned char* lds, LAS unsigned char* ldstab, const OutArgs a, const int wv) {
;     ...
;     for (int r = 0; r < 16; ++r) {
;         const int row = 32 * rb + crow(r, hi);
;         const float t1 = s1[r] + exch[((1 - dh) * 128 + row) * 2], t2 = s2[r] + exch[((1 - dh) * 128 + row) * 2 + 1];
;         float mean, inv;
;         if (MLSTM) { mean = 0.f; inv = rsqrtf(t2 * (1.f / DV) + EPS); }
;         else { mean = t1 * (1.f / DV); inv = rsqrtf(fmaxf(t2 * (1.f / DV) - mean * mean, 0.f) + EPS); }
; #pragma unroll
;         for (int nb = 0; nb < NB; ++nb) { const int col = dh * (DV / 2) + 32 * nb + r32;
;             *(LAS bf16_t*)(lds + row * TP + col * 2) = f2bf((o[nb][r] - mean) * inv); }
;     }
.LBB0_4313:
	s_or_b64 exec, exec, s[4:5]
	v_lshlrev_b32_e32 v164, 1, v219
	v_subrev_u32_e32 v164, s6, v164
	s_add_i32 s4, 0, 0x22100
	v_lshl_add_u32 v164, v164, 2, s4
	s_waitcnt vmcnt(0) lgkmcnt(0)
	s_barrier
	ds_read_b128 v[164:167], v164 offset:1024
	v_lshlrev_b32_e32 v168, 1, v217
	v_subrev_u32_e32 v168, s6, v168
	v_lshl_add_u32 v168, v168, 2, s4
	ds_read2_b64 v[168:171], v168 offset0:128 offset1:129
	s_waitcnt lgkmcnt(1)
	v_pk_add_f32 v[156:157], v[156:157], v[164:165]
	s_nop 0
	v_pk_mul_f32 v[156:157], v[156:157], s[26:27] op_sel_hi:[1,0]
	s_nop 0
	v_fma_f32 v157, -v156, v156, v157
	v_max_f32_e32 v157, 0, v157
	v_add_f32_e32 v157, 0x358637bd, v157
	v_mul_f32_e32 v164, 0x4b800000, v157
	v_cmp_gt_f32_e32 vcc, s89, v157
	v_sub_f32_e32 v16, v16, v156
	v_sub_f32_e32 v0, v0, v156
	v_cndmask_b32_e32 v157, v157, v164, vcc
	v_rsq_f32_e32 v157, v157
	v_or_b32_e32 v164, s6, v233
	v_mul_f32_e32 v165, 0x45800000, v157
	v_cndmask_b32_e32 v157, v157, v165, vcc
	v_mul_f32_e32 v16, v16, v157
	v_bfe_u32 v172, v16, 16, 1
	v_lshlrev_b32_e32 v165, 10, v219
	v_add3_u32 v172, v16, v172, s90
	v_lshlrev_b32_e32 v16, 1, v164
	v_mul_f32_e32 v0, v0, v157
	v_add3_u32 v164, 0, v165, v16
	v_bfe_u32 v165, v0, 16, 1
	v_add3_u32 v0, v0, v165, s90
	ds_write_b16_d16_hi v164, v0 offset:64
	v_sub_f32_e32 v0, v32, v156
	v_mul_f32_e32 v0, v0, v157
	v_bfe_u32 v32, v0, 16, 1
	v_add3_u32 v0, v0, v32, s90
	ds_write_b16_d16_hi v164, v0 offset:128
	v_sub_f32_e32 v0, v48, v156
	v_mul_f32_e32 v0, v0, v157
	v_bfe_u32 v32, v0, 16, 1
	v_add3_u32 v0, v0, v32, s90
	ds_write_b16_d16_hi v164, v0 offset:192
	v_sub_f32_e32 v0, v96, v156
	v_mul_f32_e32 v0, v0, v157
	v_bfe_u32 v32, v0, 16, 1
	v_add3_u32 v0, v0, v32, s90
	ds_write_b16_d16_hi v164, v0 offset:256
	v_sub_f32_e32 v0, v112, v156
	v_mul_f32_e32 v0, v0, v157
	v_bfe_u32 v32, v0, 16, 1
	v_add3_u32 v0, v0, v32, s90
	ds_write_b16_d16_hi v164, v0 offset:320
	v_sub_f32_e32 v0, v80, v156
	v_mul_f32_e32 v0, v0, v157
	v_bfe_u32 v32, v0, 16, 1
	v_add3_u32 v0, v0, v32, s90
	ds_write_b16_d16_hi v164, v0 offset:384
	v_sub_f32_e32 v0, v64, v156
	v_mul_f32_e32 v0, v0, v157
	v_pk_add_f32 v[156:157], v[158:159], v[166:167]
	ds_write_b16_d16_hi v164, v172
	v_pk_mul_f32 v[156:157], v[156:157], s[26:27] op_sel_hi:[1,0]
	s_nop 0
	v_fma_f32 v32, -v156, v156, v157
	v_max_f32_e32 v32, 0, v32
	v_add_f32_e32 v32, 0x358637bd, v32
	v_mul_f32_e32 v48, 0x4b800000, v32
	v_cmp_gt_f32_e32 vcc, s89, v32
	v_sub_f32_e32 v17, v17, v156
	v_sub_f32_e32 v1, v1, v156
	v_cndmask_b32_e32 v32, v32, v48, vcc
	v_rsq_f32_e32 v32, v32
	v_bfe_u32 v48, v0, 16, 1
	v_add3_u32 v0, v0, v48, s90
	ds_write_b16_d16_hi v164, v0 offset:448
	v_mul_f32_e32 v0, 0x45800000, v32
	v_cndmask_b32_e32 v0, v32, v0, vcc
	v_mul_f32_e32 v17, v17, v0
	v_lshlrev_b32_e32 v32, 10, v218
	v_bfe_u32 v48, v17, 16, 1
	v_add3_u32 v17, v17, v48, s90
	v_add3_u32 v32, 0, v32, v16
	v_mul_f32_e32 v1, v1, v0
	ds_write_b16_d16_hi v32, v17
	v_bfe_u32 v17, v1, 16, 1
	v_add3_u32 v1, v1, v17, s90
	ds_write_b16_d16_hi v32, v1 offset:64
	v_sub_f32_e32 v1, v33, v156
	v_mul_f32_e32 v1, v1, v0
	v_bfe_u32 v17, v1, 16, 1
	v_add3_u32 v1, v1, v17, s90
	ds_write_b16_d16_hi v32, v1 offset:128
	v_sub_f32_e32 v1, v49, v156
	v_mul_f32_e32 v1, v1, v0
	v_bfe_u32 v17, v1, 16, 1
	v_add3_u32 v1, v1, v17, s90
	ds_write_b16_d16_hi v32, v1 offset:192
	v_sub_f32_e32 v1, v97, v156
	v_mul_f32_e32 v1, v1, v0
	v_bfe_u32 v17, v1, 16, 1
	v_add3_u32 v1, v1, v17, s90
	ds_write_b16_d16_hi v32, v1 offset:256
	v_sub_f32_e32 v1, v113, v156
	v_mul_f32_e32 v1, v1, v0
	v_bfe_u32 v17, v1, 16, 1
	v_add3_u32 v1, v1, v17, s90
	ds_write_b16_d16_hi v32, v1 offset:320
	v_sub_f32_e32 v1, v81, v156
	v_mul_f32_e32 v1, v1, v0
	v_bfe_u32 v17, v1, 16, 1
	v_add3_u32 v1, v1, v17, s90
	ds_write_b16_d16_hi v32, v1 offset:384
	v_sub_f32_e32 v1, v65, v156
	v_mul_f32_e32 v17, v1, v0
	s_waitcnt lgkmcnt(14)
	v_pk_add_f32 v[0:1], v[152:153], v[168:169]
	s_nop 0
	v_pk_mul_f32 v[0:1], v[0:1], s[26:27] op_sel_hi:[1,0]
	s_nop 0
	v_fma_f32 v1, -v0, v0, v1
	v_max_f32_e32 v1, 0, v1
	v_add_f32_e32 v1, 0x358637bd, v1
	v_mul_f32_e32 v33, 0x4b800000, v1
	v_cmp_gt_f32_e32 vcc, s89, v1
	v_sub_f32_e32 v18, v18, v0
	v_sub_f32_e32 v2, v2, v0
	v_cndmask_b32_e32 v1, v1, v33, vcc
	v_rsq_f32_e32 v1, v1
	v_bfe_u32 v33, v17, 16, 1
	v_add3_u32 v17, v17, v33, s90
	ds_write_b16_d16_hi v32, v17 offset:448
	v_mul_f32_e32 v17, 0x45800000, v1
	v_cndmask_b32_e32 v1, v1, v17, vcc
	v_mul_f32_e32 v18, v18, v1
	v_lshlrev_b32_e32 v17, 10, v217
	v_bfe_u32 v32, v18, 16, 1
	v_add3_u32 v18, v18, v32, s90
	v_add3_u32 v17, 0, v17, v16
	v_mul_f32_e32 v2, v2, v1
	ds_write_b16_d16_hi v17, v18
	v_bfe_u32 v18, v2, 16, 1
	v_add3_u32 v2, v2, v18, s90
	ds_write_b16_d16_hi v17, v2 offset:64
	v_sub_f32_e32 v2, v34, v0
	v_mul_f32_e32 v2, v2, v1
	v_bfe_u32 v18, v2, 16, 1
	v_add3_u32 v2, v2, v18, s90
	ds_write_b16_d16_hi v17, v2 offset:128
	v_sub_f32_e32 v2, v50, v0
	v_mul_f32_e32 v2, v2, v1
	v_bfe_u32 v18, v2, 16, 1
	v_add3_u32 v2, v2, v18, s90
	ds_write_b16_d16_hi v17, v2 offset:192
	v_sub_f32_e32 v2, v98, v0
	v_mul_f32_e32 v2, v2, v1
	v_bfe_u32 v18, v2, 16, 1
	v_add3_u32 v2, v2, v18, s90
	ds_write_b16_d16_hi v17, v2 offset:256
	v_sub_f32_e32 v2, v114, v0
	v_mul_f32_e32 v2, v2, v1
	v_bfe_u32 v18, v2, 16, 1
	v_add3_u32 v2, v2, v18, s90
	ds_write_b16_d16_hi v17, v2 offset:320
	v_sub_f32_e32 v2, v82, v0
	v_mul_f32_e32 v2, v2, v1
	v_bfe_u32 v18, v2, 16, 1
	v_add3_u32 v2, v2, v18, s90
	v_sub_f32_e32 v0, v66, v0
	ds_write_b16_d16_hi v17, v2 offset:384
	v_mul_f32_e32 v2, v0, v1
	v_pk_add_f32 v[0:1], v[154:155], v[170:171]
	s_nop 0
	v_pk_mul_f32 v[0:1], v[0:1], s[26:27] op_sel_hi:[1,0]
	s_nop 0
	v_fma_f32 v1, -v0, v0, v1
	v_max_f32_e32 v1, 0, v1
; #define LAS __attribute__((address_space(3)))
; __device__ __forceinline__ bf16_t f2bf(float f) { unsigned u = __builtin_bit_cast(unsigned, f); return (bf16_t)((u + 0x7fffu + ((u >> 16) & 1u)) >> 16); }
; __device__ __forceinline__ int crow(int r, int hi) { return (r & 3) + 8 * (r >> 2) + 4 * hi; }
; __device__ __forceinline__ int crow(int r, int hi) { return (r & 3) + 8 * (r >> 2) + 4 * hi; }
; template <int DK, int DV, bool MLSTM>
; __device__ __forceinline__ void out_unit2(LAS unsigned char* lds, LAS unsigned char* ldstab, const OutArgs a, const int wv) {
;     ...
;     for (int r = 0; r < 16; ++r) {
;         const int row = 32 * rb + crow(r, hi);
;         const float t1 = s1[r] + exch[((1 - dh) * 128 + row) * 2], t2 = s2[r] + exch[((1 - dh) * 128 + row) * 2 + 1];
;         float mean, inv;
;         if (MLSTM) { mean = 0.f; inv = rsqrtf(t2 * (1.f / DV) + EPS); }
;         else { mean = t1 * (1.f / DV); inv = rsqrtf(fmaxf(t2 * (1.f / DV) - mean * mean, 0.f) + EPS); }
; #pragma unroll
;         for (int nb = 0; nb < NB; ++nb) { const int col = dh * (DV / 2) + 32 * nb + r32;
;             *(LAS bf16_t*)(lds + row * TP + col * 2) = f2bf((o[nb][r] - mean) * inv); }
;     }
	v_add_f32_e32 v1, 0x358637bd, v1
	v_mul_f32_e32 v18, 0x4b800000, v1
	v_cmp_gt_f32_e32 vcc, s89, v1
	s_nop 1
	v_cndmask_b32_e32 v1, v1, v18, vcc
	v_rsq_f32_e32 v1, v1
	v_bfe_u32 v18, v2, 16, 1
	v_add3_u32 v2, v2, v18, s90
	ds_write_b16_d16_hi v17, v2 offset:448
	v_mul_f32_e32 v2, 0x45800000, v1
	v_cndmask_b32_e32 v1, v1, v2, vcc
	v_sub_f32_e32 v17, v19, v0
	v_mul_f32_e32 v17, v17, v1
	v_lshlrev_b32_e32 v2, 10, v216
	v_bfe_u32 v18, v17, 16, 1
	v_add3_u32 v17, v17, v18, s90
	v_add3_u32 v18, 0, v2, v16
	v_sub_f32_e32 v2, v3, v0
	v_mul_f32_e32 v2, v2, v1
	v_bfe_u32 v3, v2, 16, 1
	v_add3_u32 v2, v2, v3, s90
	ds_write_b16_d16_hi v18, v2 offset:64
	v_sub_f32_e32 v2, v35, v0
	v_mul_f32_e32 v2, v2, v1
	v_bfe_u32 v3, v2, 16, 1
	v_add3_u32 v2, v2, v3, s90
	ds_write_b16_d16_hi v18, v2 offset:128
	v_sub_f32_e32 v2, v51, v0
	v_mul_f32_e32 v2, v2, v1
	v_bfe_u32 v3, v2, 16, 1
	v_add3_u32 v2, v2, v3, s90
	ds_write_b16_d16_hi v18, v2 offset:192
	v_sub_f32_e32 v2, v99, v0
	v_mul_f32_e32 v2, v2, v1
	v_bfe_u32 v3, v2, 16, 1
	v_add3_u32 v2, v2, v3, s90
	ds_write_b16_d16_hi v18, v2 offset:256
	v_sub_f32_e32 v2, v115, v0
	v_mul_f32_e32 v2, v2, v1
	v_bfe_u32 v3, v2, 16, 1
	v_add3_u32 v2, v2, v3, s90
	ds_write_b16_d16_hi v18, v2 offset:320
	v_sub_f32_e32 v2, v83, v0
	v_sub_f32_e32 v0, v67, v0
	ds_write_b16_d16_hi v18, v17
	v_mul_f32_e32 v2, v2, v1
	v_mul_f32_e32 v17, v0, v1
	v_lshlrev_b32_e32 v0, 1, v215
	v_bfe_u32 v3, v2, 16, 1
	v_subrev_u32_e32 v0, s6, v0
	v_add3_u32 v2, v2, v3, s90
	v_lshl_add_u32 v0, v0, 2, s4
	ds_write_b16_d16_hi v18, v2 offset:384
	ds_read2_b64 v[0:3], v0 offset0:128 offset1:129
	v_lshlrev_b32_e32 v19, 1, v213
	v_subrev_u32_e32 v19, s6, v19
	v_lshl_add_u32 v19, v19, 2, s4
	ds_read2_b64 v[32:35], v19 offset0:128 offset1:129
	s_waitcnt lgkmcnt(1)
	v_pk_add_f32 v[0:1], v[148:149], v[0:1]
	s_nop 0
	v_pk_mul_f32 v[0:1], v[0:1], s[26:27] op_sel_hi:[1,0]
	s_nop 0
	v_fma_f32 v1, -v0, v0, v1
	v_max_f32_e32 v1, 0, v1
	v_add_f32_e32 v1, 0x358637bd, v1
	v_mul_f32_e32 v19, 0x4b800000, v1
	v_cmp_gt_f32_e32 vcc, s89, v1
	v_sub_f32_e32 v4, v4, v0
	s_nop 0
	v_cndmask_b32_e32 v1, v1, v19, vcc
	v_rsq_f32_e32 v1, v1
	v_bfe_u32 v19, v17, 16, 1
	v_add3_u32 v17, v17, v19, s90
	ds_write_b16_d16_hi v18, v17 offset:448
	v_mul_f32_e32 v17, 0x45800000, v1
	v_cndmask_b32_e32 v1, v1, v17, vcc
	v_sub_f32_e32 v18, v20, v0
	v_mul_f32_e32 v18, v18, v1
	v_lshlrev_b32_e32 v17, 10, v215
	v_bfe_u32 v19, v18, 16, 1
	v_add3_u32 v18, v18, v19, s90
	v_add3_u32 v17, 0, v17, v16
	v_mul_f32_e32 v4, v4, v1
	ds_write_b16_d16_hi v17, v18
	v_bfe_u32 v18, v4, 16, 1
	v_add3_u32 v4, v4, v18, s90
	ds_write_b16_d16_hi v17, v4 offset:64
	v_sub_f32_e32 v4, v36, v0
	v_mul_f32_e32 v4, v4, v1
	v_bfe_u32 v18, v4, 16, 1
	v_add3_u32 v4, v4, v18, s90
	ds_write_b16_d16_hi v17, v4 offset:128
	v_sub_f32_e32 v4, v52, v0
	v_mul_f32_e32 v4, v4, v1
	v_bfe_u32 v18, v4, 16, 1
	v_add3_u32 v4, v4, v18, s90
	ds_write_b16_d16_hi v17, v4 offset:192
	v_sub_f32_e32 v4, v100, v0
	v_mul_f32_e32 v4, v4, v1
	v_bfe_u32 v18, v4, 16, 1
	v_add3_u32 v4, v4, v18, s90
	ds_write_b16_d16_hi v17, v4 offset:256
	v_sub_f32_e32 v4, v116, v0
	v_mul_f32_e32 v4, v4, v1
	v_bfe_u32 v18, v4, 16, 1
	v_add3_u32 v4, v4, v18, s90
	ds_write_b16_d16_hi v17, v4 offset:320
	v_sub_f32_e32 v4, v84, v0
	v_mul_f32_e32 v4, v4, v1
	v_bfe_u32 v18, v4, 16, 1
	v_add3_u32 v4, v4, v18, s90
	v_sub_f32_e32 v0, v68, v0
	ds_write_b16_d16_hi v17, v4 offset:384
	v_mul_f32_e32 v4, v0, v1
	v_pk_add_f32 v[0:1], v[150:151], v[2:3]
	s_nop 0
	v_pk_mul_f32 v[0:1], v[0:1], s[26:27] op_sel_hi:[1,0]
	s_nop 0
	v_fma_f32 v1, -v0, v0, v1
	v_max_f32_e32 v1, 0, v1
	v_add_f32_e32 v1, 0x358637bd, v1
	v_mul_f32_e32 v2, 0x4b800000, v1
	v_cmp_gt_f32_e32 vcc, s89, v1
	v_sub_f32_e32 v3, v21, v0
	s_nop 0
	v_cndmask_b32_e32 v1, v1, v2, vcc
	v_rsq_f32_e32 v1, v1
	v_bfe_u32 v2, v4, 16, 1
	v_add3_u32 v2, v4, v2, s90
	ds_write_b16_d16_hi v17, v2 offset:448
	v_mul_f32_e32 v2, 0x45800000, v1
	v_cndmask_b32_e32 v1, v1, v2, vcc
	v_mul_f32_e32 v3, v3, v1
	v_lshlrev_b32_e32 v2, 10, v214
	v_bfe_u32 v4, v3, 16, 1
	v_add3_u32 v3, v3, v4, s90
	v_add3_u32 v2, 0, v2, v16
	ds_write_b16_d16_hi v2, v3
	v_sub_f32_e32 v3, v5, v0
	v_mul_f32_e32 v3, v3, v1
	v_bfe_u32 v4, v3, 16, 1
	v_add3_u32 v3, v3, v4, s90
	ds_write_b16_d16_hi v2, v3 offset:64
	v_sub_f32_e32 v3, v37, v0
	v_mul_f32_e32 v3, v3, v1
	v_bfe_u32 v4, v3, 16, 1
	v_add3_u32 v3, v3, v4, s90
	ds_write_b16_d16_hi v2, v3 offset:128
	v_sub_f32_e32 v3, v53, v0
	v_mul_f32_e32 v3, v3, v1
	v_bfe_u32 v4, v3, 16, 1
	v_add3_u32 v3, v3, v4, s90
	ds_write_b16_d16_hi v2, v3 offset:192
	v_sub_f32_e32 v3, v101, v0
	v_mul_f32_e32 v3, v3, v1
	v_bfe_u32 v4, v3, 16, 1
	v_add3_u32 v3, v3, v4, s90
	ds_write_b16_d16_hi v2, v3 offset:256
	v_sub_f32_e32 v3, v117, v0
	v_mul_f32_e32 v3, v3, v1
	v_bfe_u32 v4, v3, 16, 1
	v_add3_u32 v3, v3, v4, s90
	ds_write_b16_d16_hi v2, v3 offset:320
	v_sub_f32_e32 v3, v85, v0
	v_mul_f32_e32 v3, v3, v1
	v_bfe_u32 v4, v3, 16, 1
	v_add3_u32 v3, v3, v4, s90
	v_sub_f32_e32 v0, v69, v0
	ds_write_b16_d16_hi v2, v3 offset:384
	v_mul_f32_e32 v3, v0, v1
	s_waitcnt lgkmcnt(14)
; #define LAS __attribute__((address_space(3)))
; __device__ __forceinline__ bf16_t f2bf(float f) { unsigned u = __builtin_bit_cast(unsigned, f); return (bf16_t)((u + 0x7fffu + ((u >> 16) & 1u)) >> 16); }
; __device__ __forceinline__ int crow(int r, int hi) { return (r & 3) + 8 * (r >> 2) + 4 * hi; }
; __device__ __forceinline__ int crow(int r, int hi) { return (r & 3) + 8 * (r >> 2) + 4 * hi; }
; template <int DK, int DV, bool MLSTM>
; __device__ __forceinline__ void out_unit2(LAS unsigned char* lds, LAS unsigned char* ldstab, const OutArgs a, const int wv) {
;     ...
;     for (int r = 0; r < 16; ++r) {
;         const int row = 32 * rb + crow(r, hi);
;         const float t1 = s1[r] + exch[((1 - dh) * 128 + row) * 2], t2 = s2[r] + exch[((1 - dh) * 128 + row) * 2 + 1];
;         float mean, inv;
;         if (MLSTM) { mean = 0.f; inv = rsqrtf(t2 * (1.f / DV) + EPS); }
;         else { mean = t1 * (1.f / DV); inv = rsqrtf(fmaxf(t2 * (1.f / DV) - mean * mean, 0.f) + EPS); }
; #pragma unroll
;         for (int nb = 0; nb < NB; ++nb) { const int col = dh * (DV / 2) + 32 * nb + r32;
;             *(LAS bf16_t*)(lds + row * TP + col * 2) = f2bf((o[nb][r] - mean) * inv); }
;     }
	v_pk_add_f32 v[0:1], v[144:145], v[32:33]
	s_nop 0
	v_pk_mul_f32 v[0:1], v[0:1], s[26:27] op_sel_hi:[1,0]
	s_nop 0
	v_fma_f32 v1, -v0, v0, v1
	v_max_f32_e32 v1, 0, v1
	v_add_f32_e32 v1, 0x358637bd, v1
	v_mul_f32_e32 v4, 0x4b800000, v1
	v_cmp_gt_f32_e32 vcc, s89, v1
	s_nop 1
	v_cndmask_b32_e32 v1, v1, v4, vcc
	v_rsq_f32_e32 v1, v1
	v_bfe_u32 v4, v3, 16, 1
	v_add3_u32 v3, v3, v4, s90
	ds_write_b16_d16_hi v2, v3 offset:448
	v_mul_f32_e32 v2, 0x45800000, v1
	v_cndmask_b32_e32 v1, v1, v2, vcc
	v_sub_f32_e32 v3, v22, v0
	v_mul_f32_e32 v3, v3, v1
	v_lshlrev_b32_e32 v2, 10, v213
	v_bfe_u32 v4, v3, 16, 1
	v_add3_u32 v3, v3, v4, s90
	v_add3_u32 v2, 0, v2, v16
	ds_write_b16_d16_hi v2, v3
	v_sub_f32_e32 v3, v6, v0
	v_mul_f32_e32 v3, v3, v1
	v_bfe_u32 v4, v3, 16, 1
	v_add3_u32 v3, v3, v4, s90
	ds_write_b16_d16_hi v2, v3 offset:64
	v_sub_f32_e32 v3, v38, v0
	v_mul_f32_e32 v3, v3, v1
	v_bfe_u32 v4, v3, 16, 1
	v_add3_u32 v3, v3, v4, s90
	ds_write_b16_d16_hi v2, v3 offset:128
	v_sub_f32_e32 v3, v54, v0
	v_mul_f32_e32 v3, v3, v1
	v_bfe_u32 v4, v3, 16, 1
	v_add3_u32 v3, v3, v4, s90
	ds_write_b16_d16_hi v2, v3 offset:192
	v_sub_f32_e32 v3, v102, v0
	v_mul_f32_e32 v3, v3, v1
	v_bfe_u32 v4, v3, 16, 1
	v_add3_u32 v3, v3, v4, s90
	ds_write_b16_d16_hi v2, v3 offset:256
	v_sub_f32_e32 v3, v118, v0
	v_mul_f32_e32 v3, v3, v1
	v_bfe_u32 v4, v3, 16, 1
	v_add3_u32 v3, v3, v4, s90
	ds_write_b16_d16_hi v2, v3 offset:320
	v_sub_f32_e32 v3, v86, v0
	v_mul_f32_e32 v3, v3, v1
	v_bfe_u32 v4, v3, 16, 1
	v_add3_u32 v3, v3, v4, s90
	v_sub_f32_e32 v0, v70, v0
	ds_write_b16_d16_hi v2, v3 offset:384
	v_mul_f32_e32 v3, v0, v1
	v_pk_add_f32 v[0:1], v[146:147], v[34:35]
	s_nop 0
	v_pk_mul_f32 v[0:1], v[0:1], s[26:27] op_sel_hi:[1,0]
	s_nop 0
	v_fma_f32 v1, -v0, v0, v1
	v_max_f32_e32 v1, 0, v1
	v_add_f32_e32 v1, 0x358637bd, v1
	v_mul_f32_e32 v4, 0x4b800000, v1
	v_cmp_gt_f32_e32 vcc, s89, v1
	s_nop 1
	v_cndmask_b32_e32 v1, v1, v4, vcc
	v_rsq_f32_e32 v1, v1
	v_bfe_u32 v4, v3, 16, 1
	v_add3_u32 v3, v3, v4, s90
	ds_write_b16_d16_hi v2, v3 offset:448
	v_mul_f32_e32 v2, 0x45800000, v1
	v_cndmask_b32_e32 v1, v1, v2, vcc
	v_sub_f32_e32 v3, v23, v0
	v_lshlrev_b32_e32 v2, 10, v212
	v_mul_f32_e32 v3, v3, v1
	v_bfe_u32 v4, v3, 16, 1
	v_add3_u32 v17, 0, v2, v16
	v_sub_f32_e32 v2, v7, v0
	v_add3_u32 v3, v3, v4, s90
	v_mul_f32_e32 v2, v2, v1
	ds_write_b16_d16_hi v17, v3
	v_bfe_u32 v3, v2, 16, 1
	v_add3_u32 v2, v2, v3, s90
	ds_write_b16_d16_hi v17, v2 offset:64
	v_sub_f32_e32 v2, v39, v0
	v_mul_f32_e32 v2, v2, v1
	v_bfe_u32 v3, v2, 16, 1
	v_add3_u32 v2, v2, v3, s90
	ds_write_b16_d16_hi v17, v2 offset:128
	v_sub_f32_e32 v2, v55, v0
	v_mul_f32_e32 v2, v2, v1
	v_bfe_u32 v3, v2, 16, 1
	v_add3_u32 v2, v2, v3, s90
	ds_write_b16_d16_hi v17, v2 offset:192
	v_sub_f32_e32 v2, v103, v0
	v_mul_f32_e32 v2, v2, v1
	v_bfe_u32 v3, v2, 16, 1
	v_add3_u32 v2, v2, v3, s90
	ds_write_b16_d16_hi v17, v2 offset:256
	v_sub_f32_e32 v2, v119, v0
	v_mul_f32_e32 v2, v2, v1
	v_bfe_u32 v3, v2, 16, 1
	v_add3_u32 v2, v2, v3, s90
	ds_write_b16_d16_hi v17, v2 offset:320
	v_sub_f32_e32 v2, v87, v0
	v_sub_f32_e32 v0, v71, v0
	v_mul_f32_e32 v2, v2, v1
	v_mul_f32_e32 v18, v0, v1
	v_lshlrev_b32_e32 v0, 1, v211
	v_bfe_u32 v3, v2, 16, 1
	v_subrev_u32_e32 v0, s6, v0
	v_add3_u32 v2, v2, v3, s90
	v_lshl_add_u32 v0, v0, 2, s4
	ds_write_b16_d16_hi v17, v2 offset:384
	ds_read2_b64 v[0:3], v0 offset0:128 offset1:129
	v_lshlrev_b32_e32 v4, 1, v209
	v_subrev_u32_e32 v4, s6, v4
	v_lshl_add_u32 v4, v4, 2, s4
	ds_read2_b64 v[4:7], v4 offset0:128 offset1:129
	s_waitcnt lgkmcnt(1)
	v_pk_add_f32 v[0:1], v[140:141], v[0:1]
	s_nop 0
	v_pk_mul_f32 v[0:1], v[0:1], s[26:27] op_sel_hi:[1,0]
	s_nop 0
	v_fma_f32 v1, -v0, v0, v1
	v_max_f32_e32 v1, 0, v1
	v_add_f32_e32 v1, 0x358637bd, v1
	v_mul_f32_e32 v19, 0x4b800000, v1
	v_cmp_gt_f32_e32 vcc, s89, v1
	v_sub_f32_e32 v8, v8, v0
	s_nop 0
	v_cndmask_b32_e32 v1, v1, v19, vcc
	v_rsq_f32_e32 v1, v1
	v_bfe_u32 v19, v18, 16, 1
	v_add3_u32 v18, v18, v19, s90
	ds_write_b16_d16_hi v17, v18 offset:448
	v_mul_f32_e32 v17, 0x45800000, v1
	v_cndmask_b32_e32 v1, v1, v17, vcc
	v_sub_f32_e32 v18, v24, v0
	v_mul_f32_e32 v18, v18, v1
	v_lshlrev_b32_e32 v17, 10, v211
	v_bfe_u32 v19, v18, 16, 1
	v_add3_u32 v18, v18, v19, s90
	v_add3_u32 v17, 0, v17, v16
	v_mul_f32_e32 v8, v8, v1
	ds_write_b16_d16_hi v17, v18
	v_bfe_u32 v18, v8, 16, 1
	v_add3_u32 v8, v8, v18, s90
	ds_write_b16_d16_hi v17, v8 offset:64
	v_sub_f32_e32 v8, v40, v0
	v_mul_f32_e32 v8, v8, v1
	v_bfe_u32 v18, v8, 16, 1
	v_add3_u32 v8, v8, v18, s90
	ds_write_b16_d16_hi v17, v8 offset:128
	v_sub_f32_e32 v8, v56, v0
	v_mul_f32_e32 v8, v8, v1
	v_bfe_u32 v18, v8, 16, 1
	v_add3_u32 v8, v8, v18, s90
	ds_write_b16_d16_hi v17, v8 offset:192
	v_sub_f32_e32 v8, v104, v0
	v_mul_f32_e32 v8, v8, v1
	v_bfe_u32 v18, v8, 16, 1
	v_add3_u32 v8, v8, v18, s90
	ds_write_b16_d16_hi v17, v8 offset:256
	v_sub_f32_e32 v8, v120, v0
	v_mul_f32_e32 v8, v8, v1
	v_bfe_u32 v18, v8, 16, 1
	v_add3_u32 v8, v8, v18, s90
	ds_write_b16_d16_hi v17, v8 offset:320
	v_sub_f32_e32 v8, v88, v0
	v_mul_f32_e32 v8, v8, v1
	v_bfe_u32 v18, v8, 16, 1
	v_add3_u32 v8, v8, v18, s90
	v_sub_f32_e32 v0, v72, v0
	ds_write_b16_d16_hi v17, v8 offset:384
	v_mul_f32_e32 v8, v0, v1
	v_pk_add_f32 v[0:1], v[142:143], v[2:3]
	s_nop 0
	v_pk_mul_f32 v[0:1], v[0:1], s[26:27] op_sel_hi:[1,0]
	s_nop 0
	v_fma_f32 v1, -v0, v0, v1
	v_max_f32_e32 v1, 0, v1
	v_add_f32_e32 v1, 0x358637bd, v1
	v_mul_f32_e32 v2, 0x4b800000, v1
	v_cmp_gt_f32_e32 vcc, s89, v1
	v_sub_f32_e32 v3, v25, v0
	s_nop 0
	v_cndmask_b32_e32 v1, v1, v2, vcc
	v_rsq_f32_e32 v1, v1
	v_bfe_u32 v2, v8, 16, 1
	v_add3_u32 v2, v8, v2, s90
	ds_write_b16_d16_hi v17, v2 offset:448
	v_mul_f32_e32 v2, 0x45800000, v1
	v_cndmask_b32_e32 v1, v1, v2, vcc
	v_mul_f32_e32 v3, v3, v1
	v_lshlrev_b32_e32 v2, 10, v210
	v_bfe_u32 v8, v3, 16, 1
	v_add3_u32 v3, v3, v8, s90
	v_add3_u32 v2, 0, v2, v16
	ds_write_b16_d16_hi v2, v3
	v_sub_f32_e32 v3, v9, v0
	v_mul_f32_e32 v3, v3, v1
	v_bfe_u32 v8, v3, 16, 1
	v_add3_u32 v3, v3, v8, s90
	ds_write_b16_d16_hi v2, v3 offset:64
	v_sub_f32_e32 v3, v41, v0
	v_mul_f32_e32 v3, v3, v1
	v_bfe_u32 v8, v3, 16, 1
	v_add3_u32 v3, v3, v8, s90
	ds_write_b16_d16_hi v2, v3 offset:128
	v_sub_f32_e32 v3, v57, v0
	v_mul_f32_e32 v3, v3, v1
	v_bfe_u32 v8, v3, 16, 1
	v_add3_u32 v3, v3, v8, s90
	ds_write_b16_d16_hi v2, v3 offset:192
	v_sub_f32_e32 v3, v105, v0
	v_mul_f32_e32 v3, v3, v1
	v_bfe_u32 v8, v3, 16, 1
	v_add3_u32 v3, v3, v8, s90
	ds_write_b16_d16_hi v2, v3 offset:256
	v_sub_f32_e32 v3, v121, v0
	v_mul_f32_e32 v3, v3, v1
	v_bfe_u32 v8, v3, 16, 1
	v_add3_u32 v3, v3, v8, s90
	ds_write_b16_d16_hi v2, v3 offset:320
	v_sub_f32_e32 v3, v89, v0
	v_mul_f32_e32 v3, v3, v1
	v_bfe_u32 v8, v3, 16, 1
	v_add3_u32 v3, v3, v8, s90
	v_sub_f32_e32 v0, v73, v0
	ds_write_b16_d16_hi v2, v3 offset:384
	v_mul_f32_e32 v3, v0, v1
	s_waitcnt lgkmcnt(14)
; #define LAS __attribute__((address_space(3)))
; __device__ __forceinline__ bf16_t f2bf(float f) { unsigned u = __builtin_bit_cast(unsigned, f); return (bf16_t)((u + 0x7fffu + ((u >> 16) & 1u)) >> 16); }
; __device__ __forceinline__ int crow(int r, int hi) { return (r & 3) + 8 * (r >> 2) + 4 * hi; }
; __device__ __forceinline__ int crow(int r, int hi) { return (r & 3) + 8 * (r >> 2) + 4 * hi; }
; template <int DK, int DV, bool MLSTM>
; __device__ __forceinline__ void out_unit2(LAS unsigned char* lds, LAS unsigned char* ldstab, const OutArgs a, const int wv) {
;     ...
;     for (int r = 0; r < 16; ++r) {
;         const int row = 32 * rb + crow(r, hi);
;         const float t1 = s1[r] + exch[((1 - dh) * 128 + row) * 2], t2 = s2[r] + exch[((1 - dh) * 128 + row) * 2 + 1];
;         float mean, inv;
;         if (MLSTM) { mean = 0.f; inv = rsqrtf(t2 * (1.f / DV) + EPS); }
;         else { mean = t1 * (1.f / DV); inv = rsqrtf(fmaxf(t2 * (1.f / DV) - mean * mean, 0.f) + EPS); }
; #pragma unroll
;         for (int nb = 0; nb < NB; ++nb) { const int col = dh * (DV / 2) + 32 * nb + r32;
;             *(LAS bf16_t*)(lds + row * TP + col * 2) = f2bf((o[nb][r] - mean) * inv); }
;     }
	v_pk_add_f32 v[0:1], v[136:137], v[4:5]
	s_nop 0
	v_pk_mul_f32 v[0:1], v[0:1], s[26:27] op_sel_hi:[1,0]
	s_nop 0
	v_fma_f32 v1, -v0, v0, v1
	v_max_f32_e32 v1, 0, v1
	v_add_f32_e32 v1, 0x358637bd, v1
	v_mul_f32_e32 v4, 0x4b800000, v1
	v_cmp_gt_f32_e32 vcc, s89, v1
	s_nop 1
	v_cndmask_b32_e32 v1, v1, v4, vcc
	v_rsq_f32_e32 v1, v1
	v_bfe_u32 v4, v3, 16, 1
	v_add3_u32 v3, v3, v4, s90
	ds_write_b16_d16_hi v2, v3 offset:448
	v_mul_f32_e32 v2, 0x45800000, v1
	v_cndmask_b32_e32 v1, v1, v2, vcc
	v_sub_f32_e32 v3, v26, v0
	v_mul_f32_e32 v3, v3, v1
	v_lshlrev_b32_e32 v2, 10, v209
	v_bfe_u32 v4, v3, 16, 1
	v_add3_u32 v3, v3, v4, s90
	v_add3_u32 v2, 0, v2, v16
	ds_write_b16_d16_hi v2, v3
	v_sub_f32_e32 v3, v10, v0
	v_mul_f32_e32 v3, v3, v1
	v_bfe_u32 v4, v3, 16, 1
	v_add3_u32 v3, v3, v4, s90
	ds_write_b16_d16_hi v2, v3 offset:64
	v_sub_f32_e32 v3, v42, v0
	v_mul_f32_e32 v3, v3, v1
	v_bfe_u32 v4, v3, 16, 1
	v_add3_u32 v3, v3, v4, s90
	ds_write_b16_d16_hi v2, v3 offset:128
	v_sub_f32_e32 v3, v58, v0
	v_mul_f32_e32 v3, v3, v1
	v_bfe_u32 v4, v3, 16, 1
	v_add3_u32 v3, v3, v4, s90
	ds_write_b16_d16_hi v2, v3 offset:192
	v_sub_f32_e32 v3, v106, v0
	v_mul_f32_e32 v3, v3, v1
	v_bfe_u32 v4, v3, 16, 1
	v_add3_u32 v3, v3, v4, s90
	ds_write_b16_d16_hi v2, v3 offset:256
	v_sub_f32_e32 v3, v122, v0
	v_mul_f32_e32 v3, v3, v1
	v_bfe_u32 v4, v3, 16, 1
	v_add3_u32 v3, v3, v4, s90
	ds_write_b16_d16_hi v2, v3 offset:320
	v_sub_f32_e32 v3, v90, v0
	v_mul_f32_e32 v3, v3, v1
	v_bfe_u32 v4, v3, 16, 1
	v_add3_u32 v3, v3, v4, s90
	v_sub_f32_e32 v0, v74, v0
	ds_write_b16_d16_hi v2, v3 offset:384
	v_mul_f32_e32 v3, v0, v1
	v_pk_add_f32 v[0:1], v[138:139], v[6:7]
	s_nop 0
	v_pk_mul_f32 v[0:1], v[0:1], s[26:27] op_sel_hi:[1,0]
	s_nop 0
	v_fma_f32 v1, -v0, v0, v1
	v_max_f32_e32 v1, 0, v1
	v_add_f32_e32 v1, 0x358637bd, v1
	v_mul_f32_e32 v4, 0x4b800000, v1
	v_cmp_gt_f32_e32 vcc, s89, v1
	s_nop 1
	v_cndmask_b32_e32 v1, v1, v4, vcc
	v_rsq_f32_e32 v1, v1
	v_bfe_u32 v4, v3, 16, 1
	v_add3_u32 v3, v3, v4, s90
	ds_write_b16_d16_hi v2, v3 offset:448
	v_mul_f32_e32 v2, 0x45800000, v1
	v_cndmask_b32_e32 v1, v1, v2, vcc
	v_sub_f32_e32 v3, v27, v0
	v_lshlrev_b32_e32 v2, 10, v208
	v_mul_f32_e32 v3, v3, v1
	v_bfe_u32 v4, v3, 16, 1
	v_add3_u32 v8, 0, v2, v16
	v_sub_f32_e32 v2, v11, v0
	v_add3_u32 v3, v3, v4, s90
	v_mul_f32_e32 v2, v2, v1
	ds_write_b16_d16_hi v8, v3
	v_bfe_u32 v3, v2, 16, 1
	v_add3_u32 v2, v2, v3, s90
	ds_write_b16_d16_hi v8, v2 offset:64
	v_sub_f32_e32 v2, v43, v0
	v_mul_f32_e32 v2, v2, v1
	v_bfe_u32 v3, v2, 16, 1
	v_add3_u32 v2, v2, v3, s90
	ds_write_b16_d16_hi v8, v2 offset:128
	v_sub_f32_e32 v2, v59, v0
	v_mul_f32_e32 v2, v2, v1
	v_bfe_u32 v3, v2, 16, 1
	v_add3_u32 v2, v2, v3, s90
	ds_write_b16_d16_hi v8, v2 offset:192
	v_sub_f32_e32 v2, v107, v0
	v_mul_f32_e32 v2, v2, v1
	v_bfe_u32 v3, v2, 16, 1
	v_add3_u32 v2, v2, v3, s90
	ds_write_b16_d16_hi v8, v2 offset:256
	v_sub_f32_e32 v2, v123, v0
	v_mul_f32_e32 v2, v2, v1
	v_bfe_u32 v3, v2, 16, 1
	v_add3_u32 v2, v2, v3, s90
	ds_write_b16_d16_hi v8, v2 offset:320
	v_sub_f32_e32 v2, v91, v0
	v_sub_f32_e32 v0, v75, v0
	v_mul_f32_e32 v2, v2, v1
	v_mul_f32_e32 v9, v0, v1
	v_lshlrev_b32_e32 v0, 1, v207
	v_bfe_u32 v3, v2, 16, 1
	v_subrev_u32_e32 v0, s6, v0
	v_add3_u32 v2, v2, v3, s90
	v_lshl_add_u32 v0, v0, 2, s4
	ds_write_b16_d16_hi v8, v2 offset:384
	ds_read2_b64 v[0:3], v0 offset0:128 offset1:129
	v_lshlrev_b32_e32 v4, 1, v162
	v_subrev_u32_e32 v4, s6, v4
	v_lshl_add_u32 v4, v4, 2, s4
	ds_read2_b64 v[4:7], v4 offset0:128 offset1:129
	s_waitcnt lgkmcnt(1)
	v_pk_add_f32 v[0:1], v[132:133], v[0:1]
	s_nop 0
	v_pk_mul_f32 v[0:1], v[0:1], s[26:27] op_sel_hi:[1,0]
	s_nop 0
	v_fma_f32 v1, -v0, v0, v1
	v_max_f32_e32 v1, 0, v1
	v_add_f32_e32 v1, 0x358637bd, v1
	v_mul_f32_e32 v10, 0x4b800000, v1
	v_cmp_gt_f32_e32 vcc, s89, v1
	s_nop 1
	v_cndmask_b32_e32 v1, v1, v10, vcc
	v_rsq_f32_e32 v1, v1
	v_bfe_u32 v10, v9, 16, 1
	v_add3_u32 v9, v9, v10, s90
	ds_write_b16_d16_hi v8, v9 offset:448
	v_mul_f32_e32 v8, 0x45800000, v1
	v_cndmask_b32_e32 v1, v1, v8, vcc
	v_sub_f32_e32 v9, v28, v0
	v_mul_f32_e32 v9, v9, v1
	v_lshlrev_b32_e32 v8, 10, v207
	v_bfe_u32 v10, v9, 16, 1
	v_add3_u32 v9, v9, v10, s90
	v_add3_u32 v8, 0, v8, v16
	ds_write_b16_d16_hi v8, v9
	v_sub_f32_e32 v9, v12, v0
	v_mul_f32_e32 v9, v9, v1
	v_bfe_u32 v10, v9, 16, 1
	v_add3_u32 v9, v9, v10, s90
	ds_write_b16_d16_hi v8, v9 offset:64
	v_sub_f32_e32 v9, v44, v0
	v_mul_f32_e32 v9, v9, v1
	v_bfe_u32 v10, v9, 16, 1
	v_add3_u32 v9, v9, v10, s90
	ds_write_b16_d16_hi v8, v9 offset:128
	v_sub_f32_e32 v9, v60, v0
	v_mul_f32_e32 v9, v9, v1
	v_bfe_u32 v10, v9, 16, 1
	v_add3_u32 v9, v9, v10, s90
	ds_write_b16_d16_hi v8, v9 offset:192
	v_sub_f32_e32 v9, v108, v0
	v_mul_f32_e32 v9, v9, v1
	v_bfe_u32 v10, v9, 16, 1
	v_add3_u32 v9, v9, v10, s90
	ds_write_b16_d16_hi v8, v9 offset:256
	v_sub_f32_e32 v9, v124, v0
	v_mul_f32_e32 v9, v9, v1
	v_bfe_u32 v10, v9, 16, 1
	v_add3_u32 v9, v9, v10, s90
	ds_write_b16_d16_hi v8, v9 offset:320
	v_sub_f32_e32 v9, v92, v0
	v_mul_f32_e32 v9, v9, v1
	v_bfe_u32 v10, v9, 16, 1
	v_add3_u32 v9, v9, v10, s90
	v_sub_f32_e32 v0, v76, v0
	ds_write_b16_d16_hi v8, v9 offset:384
	v_mul_f32_e32 v9, v0, v1
	v_pk_add_f32 v[0:1], v[134:135], v[2:3]
	s_nop 0
	v_pk_mul_f32 v[0:1], v[0:1], s[26:27] op_sel_hi:[1,0]
	s_nop 0
	v_fma_f32 v1, -v0, v0, v1
	v_max_f32_e32 v1, 0, v1
	v_add_f32_e32 v1, 0x358637bd, v1
	v_mul_f32_e32 v2, 0x4b800000, v1
	v_cmp_gt_f32_e32 vcc, s89, v1
	v_sub_f32_e32 v3, v29, v0
	s_nop 0
	v_cndmask_b32_e32 v1, v1, v2, vcc
	v_rsq_f32_e32 v1, v1
	v_bfe_u32 v2, v9, 16, 1
	v_add3_u32 v2, v9, v2, s90
	ds_write_b16_d16_hi v8, v2 offset:448
	v_mul_f32_e32 v2, 0x45800000, v1
	v_cndmask_b32_e32 v1, v1, v2, vcc
	v_mul_f32_e32 v3, v3, v1
	v_lshlrev_b32_e32 v2, 10, v206
	v_bfe_u32 v8, v3, 16, 1
	v_add3_u32 v3, v3, v8, s90
	v_add3_u32 v2, 0, v2, v16
	ds_write_b16_d16_hi v2, v3
	v_sub_f32_e32 v3, v13, v0
	v_mul_f32_e32 v3, v3, v1
	v_bfe_u32 v8, v3, 16, 1
	v_add3_u32 v3, v3, v8, s90
	ds_write_b16_d16_hi v2, v3 offset:64
	v_sub_f32_e32 v3, v45, v0
	v_mul_f32_e32 v3, v3, v1
	v_bfe_u32 v8, v3, 16, 1
	v_add3_u32 v3, v3, v8, s90
	ds_write_b16_d16_hi v2, v3 offset:128
	v_sub_f32_e32 v3, v61, v0
	v_mul_f32_e32 v3, v3, v1
	v_bfe_u32 v8, v3, 16, 1
	v_add3_u32 v3, v3, v8, s90
	ds_write_b16_d16_hi v2, v3 offset:192
	v_sub_f32_e32 v3, v109, v0
	v_mul_f32_e32 v3, v3, v1
	v_bfe_u32 v8, v3, 16, 1
	v_add3_u32 v3, v3, v8, s90
	ds_write_b16_d16_hi v2, v3 offset:256
	v_sub_f32_e32 v3, v125, v0
	v_mul_f32_e32 v3, v3, v1
	v_bfe_u32 v8, v3, 16, 1
	v_add3_u32 v3, v3, v8, s90
	ds_write_b16_d16_hi v2, v3 offset:320
	v_sub_f32_e32 v3, v93, v0
	v_mul_f32_e32 v3, v3, v1
	v_bfe_u32 v8, v3, 16, 1
	v_add3_u32 v3, v3, v8, s90
	v_sub_f32_e32 v0, v77, v0
	ds_write_b16_d16_hi v2, v3 offset:384
	v_mul_f32_e32 v3, v0, v1
	s_waitcnt lgkmcnt(14)
; #define LAS __attribute__((address_space(3)))
; __device__ __forceinline__ bf16_t f2bf(float f) { unsigned u = __builtin_bit_cast(unsigned, f); return (bf16_t)((u + 0x7fffu + ((u >> 16) & 1u)) >> 16); }
; template <int DK, int DV, bool MLSTM>
; __device__ __forceinline__ void out_unit2(LAS unsigned char* lds, LAS unsigned char* ldstab, const OutArgs a, const int wv) {
;     ...
;         for (int nb = 0; nb < NB; ++nb) { const int col = dh * (DV / 2) + 32 * nb + r32;
;             *(LAS bf16_t*)(lds + row * TP + col * 2) = f2bf((o[nb][r] - mean) * inv); }
;     }
;     __syncthreads();
;     constexpr int CPR = DV / 8;
; #pragma unroll 1
;     for (int id = tid; id < 128 * CPR; id += 512) { const int row = id / CPR, ch = id % CPR;
;         const u32x4 y = *(const LAS u32x4*)(lds + row * TP + ch * 16);
;         const f32x4 g0 = *(const f32x4*)(a.gain + 8 * ch), g1 = *(const f32x4*)(a.gain + 8 * ch + 4);
;         float yv[8] = {bf_lo(y.x), bf_hi(y.x), bf_lo(y.y), bf_hi(y.y), bf_lo(y.z), bf_hi(y.z), bf_lo(y.w), bf_hi(y.w)};
;         float gv[8];
;         if (MLSTM) { const u32x4 g = *(const u32x4*)(a.G + (size_t)row * a.ldg + 8 * ch);
;             gv[0] = bf_lo(g.x); gv[1] = bf_hi(g.x); gv[2] = bf_lo(g.y); gv[3] = bf_hi(g.y); gv[4] = bf_lo(g.z); gv[5] = bf_hi(g.z); gv[6] = bf_lo(g.w); gv[7] = bf_hi(g.w); }
;         else { const u32x2 g = *(const u32x2*)(a.G8 + (size_t)row * a.ldg8 + 8 * ch);
;             const f32x2 e0 = __builtin_amdgcn_cvt_pk_f32_fp8((int)g.x, false), e1 = __builtin_amdgcn_cvt_pk_f32_fp8((int)g.x, true), e2 = __builtin_amdgcn_cvt_pk_f32_fp8((int)g.y, false), e3 = __builtin_amdgcn_cvt_pk_f32_fp8((int)g.y, true);
;             gv[0] = e0[0] * a.g8inv; gv[1] = e0[1] * a.g8inv; gv[2] = e1[0] * a.g8inv; gv[3] = e1[1] * a.g8inv; gv[4] = e2[0] * a.g8inv; gv[5] = e2[1] * a.g8inv; gv[6] = e3[0] * a.g8inv; gv[7] = e3[1] * a.g8inv; }
;         float gn[8] = {g0[0], g0[1], g0[2], g0[3], g1[0], g1[1], g1[2], g1[3]};
;         float ov[8];
; #pragma unroll
;         for (int i = 0; i < 8; ++i) ov[i] = yv[i] * gn[i] * (MLSTM ? sigmoidf_(gv[i]) : siluf_(gv[i]));
;         u32x2 w; w.x = pg8::pk4_fp8c(ov[0] * a.oscale, ov[1] * a.oscale, ov[2] * a.oscale, ov[3] * a.oscale); w.y = pg8::pk4_fp8c(ov[4] * a.oscale, ov[5] * a.oscale, ov[6] * a.oscale, ov[7] * a.oscale);
;         *(u32x2*)(a.Out + (size_t)row * a.ldo + 8 * ch) = w; }
	v_pk_add_f32 v[0:1], v[128:129], v[4:5]
	s_nop 0
	v_pk_mul_f32 v[0:1], v[0:1], s[26:27] op_sel_hi:[1,0]
	s_nop 0
	v_fma_f32 v1, -v0, v0, v1
	v_max_f32_e32 v1, 0, v1
	v_add_f32_e32 v1, 0x358637bd, v1
	v_mul_f32_e32 v4, 0x4b800000, v1
	v_cmp_gt_f32_e32 vcc, s89, v1
	s_nop 1
	v_cndmask_b32_e32 v1, v1, v4, vcc
	v_rsq_f32_e32 v1, v1
	v_bfe_u32 v4, v3, 16, 1
	v_add3_u32 v3, v3, v4, s90
	ds_write_b16_d16_hi v2, v3 offset:448
	v_mul_f32_e32 v2, 0x45800000, v1
	v_cndmask_b32_e32 v1, v1, v2, vcc
	v_sub_f32_e32 v3, v30, v0
	v_mul_f32_e32 v3, v3, v1
	v_lshlrev_b32_e32 v2, 10, v162
	v_bfe_u32 v4, v3, 16, 1
	v_add3_u32 v3, v3, v4, s90
	v_add3_u32 v2, 0, v2, v16
	ds_write_b16_d16_hi v2, v3
	v_sub_f32_e32 v3, v14, v0
	v_mul_f32_e32 v3, v3, v1
	v_bfe_u32 v4, v3, 16, 1
	v_add3_u32 v3, v3, v4, s90
	ds_write_b16_d16_hi v2, v3 offset:64
	v_sub_f32_e32 v3, v46, v0
	v_mul_f32_e32 v3, v3, v1
	v_bfe_u32 v4, v3, 16, 1
	v_add3_u32 v3, v3, v4, s90
	ds_write_b16_d16_hi v2, v3 offset:128
	v_sub_f32_e32 v3, v62, v0
	v_mul_f32_e32 v3, v3, v1
	v_bfe_u32 v4, v3, 16, 1
	v_add3_u32 v3, v3, v4, s90
	ds_write_b16_d16_hi v2, v3 offset:192
	v_sub_f32_e32 v3, v110, v0
	v_mul_f32_e32 v3, v3, v1
	v_bfe_u32 v4, v3, 16, 1
	v_add3_u32 v3, v3, v4, s90
	ds_write_b16_d16_hi v2, v3 offset:256
	v_sub_f32_e32 v3, v126, v0
	v_mul_f32_e32 v3, v3, v1
	v_bfe_u32 v4, v3, 16, 1
	v_add3_u32 v3, v3, v4, s90
	ds_write_b16_d16_hi v2, v3 offset:320
	v_sub_f32_e32 v3, v94, v0
	v_mul_f32_e32 v3, v3, v1
	v_bfe_u32 v4, v3, 16, 1
	v_add3_u32 v3, v3, v4, s90
	v_sub_f32_e32 v0, v78, v0
	ds_write_b16_d16_hi v2, v3 offset:384
	v_mul_f32_e32 v3, v0, v1
	v_pk_add_f32 v[0:1], v[130:131], v[6:7]
	s_nop 0
	v_pk_mul_f32 v[0:1], v[0:1], s[26:27] op_sel_hi:[1,0]
	s_nop 0
	v_fma_f32 v1, -v0, v0, v1
	v_max_f32_e32 v1, 0, v1
	v_add_f32_e32 v1, 0x358637bd, v1
	v_mul_f32_e32 v4, 0x4b800000, v1
	v_cmp_gt_f32_e32 vcc, s89, v1
	s_nop 1
	v_cndmask_b32_e32 v1, v1, v4, vcc
	v_rsq_f32_e32 v1, v1
	v_bfe_u32 v4, v3, 16, 1
	v_add3_u32 v3, v3, v4, s90
	ds_write_b16_d16_hi v2, v3 offset:448
	v_mul_f32_e32 v2, 0x45800000, v1
	v_cndmask_b32_e32 v1, v1, v2, vcc
	v_sub_f32_e32 v3, v31, v0
	v_mul_f32_e32 v3, v3, v1
	v_lshlrev_b32_e32 v2, 10, v160
	v_bfe_u32 v4, v3, 16, 1
	v_add3_u32 v3, v3, v4, s90
	v_add3_u32 v2, 0, v2, v16
	ds_write_b16_d16_hi v2, v3
	v_sub_f32_e32 v3, v15, v0
	v_mul_f32_e32 v3, v3, v1
	v_bfe_u32 v4, v3, 16, 1
	v_add3_u32 v3, v3, v4, s90
	ds_write_b16_d16_hi v2, v3 offset:64
	v_sub_f32_e32 v3, v47, v0
	v_mul_f32_e32 v3, v3, v1
	v_bfe_u32 v4, v3, 16, 1
	v_add3_u32 v3, v3, v4, s90
	ds_write_b16_d16_hi v2, v3 offset:128
	v_sub_f32_e32 v3, v63, v0
	v_mul_f32_e32 v3, v3, v1
	v_bfe_u32 v4, v3, 16, 1
	v_add3_u32 v3, v3, v4, s90
	ds_write_b16_d16_hi v2, v3 offset:192
	v_sub_f32_e32 v3, v111, v0
	v_mul_f32_e32 v3, v3, v1
	v_bfe_u32 v4, v3, 16, 1
	v_add3_u32 v3, v3, v4, s90
	ds_write_b16_d16_hi v2, v3 offset:256
	v_sub_f32_e32 v3, v127, v0
	v_mul_f32_e32 v3, v3, v1
	v_bfe_u32 v4, v3, 16, 1
	v_add3_u32 v3, v3, v4, s90
	ds_write_b16_d16_hi v2, v3 offset:320
	v_sub_f32_e32 v3, v95, v0
	v_sub_f32_e32 v0, v79, v0
	v_mul_f32_e32 v3, v3, v1
	v_mul_f32_e32 v0, v0, v1
	v_bfe_u32 v4, v3, 16, 1
	v_bfe_u32 v1, v0, 16, 1
	v_add3_u32 v3, v3, v4, s90
	v_add3_u32 v0, v0, v1, s90
	v_cmp_gt_i32_e32 vcc, s88, v232
	ds_write_b16_d16_hi v2, v3 offset:384
	ds_write_b16_d16_hi v2, v0 offset:448
	s_waitcnt lgkmcnt(0)
	s_barrier
	s_and_saveexec_b64 s[36:37], vcc
	s_cbranch_execz .LBB0_4301
	s_lshl_b32 s4, s8, 2
	s_add_u32 s38, s51, s4
	s_addc_u32 s39, s52, 0
	s_lshl_b64 s[2:3], s[2:3], 11
	s_add_u32 s4, s53, s2
	s_addc_u32 s5, s54, s3
	s_add_u32 s40, s4, s8
	s_addc_u32 s41, s5, 0
	s_add_u32 s2, s55, s2
	s_addc_u32 s3, s56, s3
	s_add_u32 s42, s2, s8
	s_addc_u32 s43, s3, 0
	v_lshl_add_u32 v4, v232, 4, 0
	v_lshlrev_b32_e32 v5, 3, v232
	s_mov_b64 s[44:45], 0
	v_and_b32_e32 v6, 63, v232
	v_lshrrev_b32_e32 v7, 6, v232
	v_lshlrev_b32_e32 v8, 5, v6
	v_lshlrev_b32_e32 v5, 3, v6
	v_lshl_add_u32 v5, v7, 11, v5
	ds_read_b128 v[0:3], v4
	v_add_u32_e32 v4, 0x2000, v4
	global_load_dwordx4 v[40:43], v8, s[38:39]
	global_load_dwordx4 v[44:47], v8, s[38:39] offset:16
	global_load_dwordx2 v[30:31], v5, s[40:41]
	v_add_u32_e32 v23, 0x4000, v5
	s_nop 0
	global_load_dwordx2 v[6:7], v23, s[40:41]
	v_add_u32_e32 v23, 0x4000, v23
	v_mov_b32_e32 v162, v163
	s_mov_b32 s98, 0xbfb8aa3b
	s_mov_b32 s100, 0x41800000
	s_movk_i32 s44, 8
	s_waitcnt vmcnt(1)
.Ldloop1:
	s_waitcnt vmcnt(2) lgkmcnt(0)
	v_lshlrev_b32_e32 v10, 16, v0
	v_and_b32_e32 v11, 0xffff0000, v0
	v_lshlrev_b32_e32 v12, 16, v1
	v_and_b32_e32 v13, 0xffff0000, v1
	v_lshlrev_b32_e32 v14, 16, v2
	v_and_b32_e32 v15, 0xffff0000, v2
	v_lshlrev_b32_e32 v16, 16, v3
	v_and_b32_e32 v17, 0xffff0000, v3
	v_cvt_pk_f32_fp8_e32 v[32:33], v30
	v_cvt_pk_f32_fp8_sdwa v[34:35], v30 src0_sel:WORD_1
	v_cvt_pk_f32_fp8_e32 v[36:37], v31
	v_cvt_pk_f32_fp8_sdwa v[38:39], v31 src0_sel:WORD_1
	ds_read_b128 v[0:3], v4
	v_add_u32_e32 v4, 0x2000, v4
	s_cmp_eq_u32 s44, 1
	s_cbranch_scc1 .Ldloop1a
	global_load_dwordx2 v[30:31], v23, s[40:41]
	v_add_u32_e32 v23, 0x4000, v23
; #define LAS __attribute__((address_space(3)))
; __device__ __forceinline__ float sigmoidf_(float x) { return 1.f / (1.f + __expf(-x)); }
; __device__ __forceinline__ float siluf_(float x) { return x / (1.f + __expf(-x)); }
; __device__ __forceinline__ unsigned pk4_fp8c(float a, float b, float c, float d) { return pk4_fp8(__builtin_amdgcn_fmed3f(a, -448.f, 448.f), __builtin_amdgcn_fmed3f(b, -448.f, 448.f), __builtin_amdgcn_fmed3f(c, -448.f, 448.f), __builtin_amdgcn_fmed3f(d, -448.f, 448.f)); }
; template <int DK, int DV, bool MLSTM>
; __device__ __forceinline__ void out_unit2(LAS unsigned char* lds, LAS unsigned char* ldstab, const OutArgs a, const int wv) {
;     ...
;     for (int id = tid; id < 128 * CPR; id += 512) { const int row = id / CPR, ch = id % CPR;
;         const u32x4 y = *(const LAS u32x4*)(lds + row * TP + ch * 16);
;         const f32x4 g0 = *(const f32x4*)(a.gain + 8 * ch), g1 = *(const f32x4*)(a.gain + 8 * ch + 4);
;         float yv[8] = {bf_lo(y.x), bf_hi(y.x), bf_lo(y.y), bf_hi(y.y), bf_lo(y.z), bf_hi(y.z), bf_lo(y.w), bf_hi(y.w)};
;         float gv[8];
;         if (MLSTM) { const u32x4 g = *(const u32x4*)(a.G + (size_t)row * a.ldg + 8 * ch);
;             gv[0] = bf_lo(g.x); gv[1] = bf_hi(g.x); gv[2] = bf_lo(g.y); gv[3] = bf_hi(g.y); gv[4] = bf_lo(g.z); gv[5] = bf_hi(g.z); gv[6] = bf_lo(g.w); gv[7] = bf_hi(g.w); }
;         else { const u32x2 g = *(const u32x2*)(a.G8 + (size_t)row * a.ldg8 + 8 * ch);
;             const f32x2 e0 = __builtin_amdgcn_cvt_pk_f32_fp8((int)g.x, false), e1 = __builtin_amdgcn_cvt_pk_f32_fp8((int)g.x, true), e2 = __builtin_amdgcn_cvt_pk_f32_fp8((int)g.y, false), e3 = __builtin_amdgcn_cvt_pk_f32_fp8((int)g.y, true);
;             gv[0] = e0[0] * a.g8inv; gv[1] = e0[1] * a.g8inv; gv[2] = e1[0] * a.g8inv; gv[3] = e1[1] * a.g8inv; gv[4] = e2[0] * a.g8inv; gv[5] = e2[1] * a.g8inv; gv[6] = e3[0] * a.g8inv; gv[7] = e3[1] * a.g8inv; }
;         float gn[8] = {g0[0], g0[1], g0[2], g0[3], g1[0], g1[1], g1[2], g1[3]};
;         float ov[8];
; #pragma unroll
;         for (int i = 0; i < 8; ++i) ov[i] = yv[i] * gn[i] * (MLSTM ? sigmoidf_(gv[i]) : siluf_(gv[i]));
;         u32x2 w; w.x = pg8::pk4_fp8c(ov[0] * a.oscale, ov[1] * a.oscale, ov[2] * a.oscale, ov[3] * a.oscale); w.y = pg8::pk4_fp8c(ov[4] * a.oscale, ov[5] * a.oscale, ov[6] * a.oscale, ov[7] * a.oscale);
;         *(u32x2*)(a.Out + (size_t)row * a.ldo + 8 * ch) = w; }
.Ldloop1a:
	v_pk_mul_f32 v[10:11], v[40:41], v[10:11]
	v_pk_mul_f32 v[12:13], v[42:43], v[12:13]
	v_pk_mul_f32 v[14:15], v[44:45], v[14:15]
	v_pk_mul_f32 v[16:17], v[46:47], v[16:17]
	v_pk_mul_f32 v[32:33], v[32:33], v[162:163]
	v_pk_mul_f32 v[34:35], v[34:35], v[162:163]
	v_pk_mul_f32 v[36:37], v[36:37], v[162:163]
	v_pk_mul_f32 v[38:39], v[38:39], v[162:163]
	v_pk_mul_f32 v[48:49], v[32:33], s[98:99] op_sel_hi:[1,0]
	v_pk_mul_f32 v[50:51], v[34:35], s[98:99] op_sel_hi:[1,0]
	v_pk_mul_f32 v[52:53], v[36:37], s[98:99] op_sel_hi:[1,0]
	v_pk_mul_f32 v[54:55], v[38:39], s[98:99] op_sel_hi:[1,0]
	v_exp_f32_e32 v48, v48
	v_exp_f32_e32 v49, v49
	v_exp_f32_e32 v50, v50
	v_exp_f32_e32 v51, v51
	v_exp_f32_e32 v52, v52
	v_exp_f32_e32 v53, v53
	v_exp_f32_e32 v54, v54
	v_exp_f32_e32 v55, v55
	v_pk_add_f32 v[48:49], v[48:49], 1.0 op_sel_hi:[1,0]
	v_pk_add_f32 v[50:51], v[50:51], 1.0 op_sel_hi:[1,0]
	v_pk_add_f32 v[52:53], v[52:53], 1.0 op_sel_hi:[1,0]
	v_pk_add_f32 v[54:55], v[54:55], 1.0 op_sel_hi:[1,0]
	v_rcp_f32_e32 v56, v48
	v_rcp_f32_e32 v57, v49
	v_rcp_f32_e32 v58, v50
	v_rcp_f32_e32 v59, v51
	v_rcp_f32_e32 v60, v52
	v_rcp_f32_e32 v61, v53
	v_rcp_f32_e32 v62, v54
	v_rcp_f32_e32 v63, v55
	v_pk_fma_f32 v[8:9], v[48:49], v[56:57], 1.0 op_sel_hi:[1,1,0] neg_lo:[1,0,0] neg_hi:[1,0,0]
	v_pk_fma_f32 v[18:19], v[50:51], v[58:59], 1.0 op_sel_hi:[1,1,0] neg_lo:[1,0,0] neg_hi:[1,0,0]
	v_pk_fma_f32 v[20:21], v[52:53], v[60:61], 1.0 op_sel_hi:[1,1,0] neg_lo:[1,0,0] neg_hi:[1,0,0]
	v_pk_fma_f32 v[26:27], v[54:55], v[62:63], 1.0 op_sel_hi:[1,1,0] neg_lo:[1,0,0] neg_hi:[1,0,0]
	v_pk_fma_f32 v[56:57], v[8:9], v[56:57], v[56:57]
	v_pk_fma_f32 v[58:59], v[18:19], v[58:59], v[58:59]
	v_pk_fma_f32 v[60:61], v[20:21], v[60:61], v[60:61]
	v_pk_fma_f32 v[62:63], v[26:27], v[62:63], v[62:63]
	v_pk_mul_f32 v[64:65], v[32:33], v[56:57]
	v_pk_mul_f32 v[66:67], v[34:35], v[58:59]
	v_pk_mul_f32 v[68:69], v[36:37], v[60:61]
	v_pk_mul_f32 v[70:71], v[38:39], v[62:63]
	v_pk_fma_f32 v[8:9], v[48:49], v[64:65], v[32:33] neg_lo:[1,0,0] neg_hi:[1,0,0]
	v_pk_fma_f32 v[18:19], v[50:51], v[66:67], v[34:35] neg_lo:[1,0,0] neg_hi:[1,0,0]
	v_pk_fma_f32 v[20:21], v[52:53], v[68:69], v[36:37] neg_lo:[1,0,0] neg_hi:[1,0,0]
	v_pk_fma_f32 v[26:27], v[54:55], v[70:71], v[38:39] neg_lo:[1,0,0] neg_hi:[1,0,0]
	v_pk_fma_f32 v[64:65], v[8:9], v[56:57], v[64:65]
	v_pk_fma_f32 v[66:67], v[18:19], v[58:59], v[66:67]
	v_pk_fma_f32 v[68:69], v[20:21], v[60:61], v[68:69]
	v_pk_fma_f32 v[70:71], v[26:27], v[62:63], v[70:71]
	v_pk_fma_f32 v[8:9], v[48:49], v[64:65], v[32:33] neg_lo:[1,0,0] neg_hi:[1,0,0]
	v_pk_fma_f32 v[18:19], v[50:51], v[66:67], v[34:35] neg_lo:[1,0,0] neg_hi:[1,0,0]
	v_pk_fma_f32 v[20:21], v[52:53], v[68:69], v[36:37] neg_lo:[1,0,0] neg_hi:[1,0,0]
	v_pk_fma_f32 v[26:27], v[54:55], v[70:71], v[38:39] neg_lo:[1,0,0] neg_hi:[1,0,0]
	v_pk_fma_f32 v[8:9], v[8:9], v[56:57], v[64:65]
	v_pk_fma_f32 v[18:19], v[18:19], v[58:59], v[66:67]
	v_pk_fma_f32 v[20:21], v[20:21], v[60:61], v[68:69]
	v_pk_fma_f32 v[26:27], v[26:27], v[62:63], v[70:71]
	v_div_fixup_f32 v8, v8, v48, v32
	v_div_fixup_f32 v9, v9, v49, v33
	v_div_fixup_f32 v18, v18, v50, v34
	v_div_fixup_f32 v19, v19, v51, v35
	v_div_fixup_f32 v20, v20, v52, v36
	v_div_fixup_f32 v21, v21, v53, v37
	v_div_fixup_f32 v26, v26, v54, v38
	v_div_fixup_f32 v27, v27, v55, v39
	v_pk_mul_f32 v[10:11], v[10:11], v[8:9]
	v_pk_mul_f32 v[12:13], v[12:13], v[18:19]
	v_pk_mul_f32 v[14:15], v[14:15], v[20:21]
	v_pk_mul_f32 v[16:17], v[16:17], v[26:27]
	v_pk_mul_f32 v[10:11], v[10:11], s[100:101] op_sel_hi:[1,0]
	v_pk_mul_f32 v[12:13], v[12:13], s[100:101] op_sel_hi:[1,0]
	v_pk_mul_f32 v[14:15], v[14:15], s[100:101] op_sel_hi:[1,0]
	v_pk_mul_f32 v[16:17], v[16:17], s[100:101] op_sel_hi:[1,0]
	v_med3_f32 v10, v10, s91, v231
	v_med3_f32 v11, v11, s91, v231
	v_med3_f32 v12, v12, s91, v231
	v_med3_f32 v13, v13, s91, v231
	v_med3_f32 v14, v14, s91, v231
	v_med3_f32 v15, v15, s91, v231
	v_med3_f32 v16, v16, s91, v231
	v_med3_f32 v17, v17, s91, v231
	v_cvt_pk_fp8_f32 v24, v10, v11
	v_cvt_pk_fp8_f32 v25, v14, v15
	s_nop 0
	v_cvt_pk_fp8_f32 v24, v12, v13 op_sel:[0,0,1]
	v_cvt_pk_fp8_f32 v25, v16, v17 op_sel:[0,0,1]
	s_nop 0
	global_store_dwordx2 v5, v[24:25], s[42:43]
	v_add_u32_e32 v5, 0x4000, v5
	s_waitcnt vmcnt(2) lgkmcnt(0)
	v_lshlrev_b32_e32 v10, 16, v0
	v_and_b32_e32 v11, 0xffff0000, v0
	v_lshlrev_b32_e32 v12, 16, v1
	v_and_b32_e32 v13, 0xffff0000, v1
	v_lshlrev_b32_e32 v14, 16, v2
	v_and_b32_e32 v15, 0xffff0000, v2
	v_lshlrev_b32_e32 v16, 16, v3
	v_and_b32_e32 v17, 0xffff0000, v3
	v_cvt_pk_f32_fp8_e32 v[32:33], v6
	v_cvt_pk_f32_fp8_sdwa v[34:35], v6 src0_sel:WORD_1
	v_cvt_pk_f32_fp8_e32 v[36:37], v7
	v_cvt_pk_f32_fp8_sdwa v[38:39], v7 src0_sel:WORD_1
	ds_read_b128 v[0:3], v4
	v_add_u32_e32 v4, 0x2000, v4
	s_cmp_eq_u32 s44, 1
	s_cbranch_scc1 .Ldloop1b
	global_load_dwordx2 v[6:7], v23, s[40:41]
	v_add_u32_e32 v23, 0x4000, v23
; #define LAS __attribute__((address_space(3)))
; __device__ __forceinline__ float sigmoidf_(float x) { return 1.f / (1.f + __expf(-x)); }
; __device__ __forceinline__ float siluf_(float x) { return x / (1.f + __expf(-x)); }
; __device__ __forceinline__ unsigned pk4_fp8c(float a, float b, float c, float d) { return pk4_fp8(__builtin_amdgcn_fmed3f(a, -448.f, 448.f), __builtin_amdgcn_fmed3f(b, -448.f, 448.f), __builtin_amdgcn_fmed3f(c, -448.f, 448.f), __builtin_amdgcn_fmed3f(d, -448.f, 448.f)); }
; template <int DK, int DV, bool MLSTM>
; __device__ __forceinline__ void out_unit2(LAS unsigned char* lds, LAS unsigned char* ldstab, const OutArgs a, const int wv) {
;     ...
;     for (int id = tid; id < 128 * CPR; id += 512) { const int row = id / CPR, ch = id % CPR;
;         const u32x4 y = *(const LAS u32x4*)(lds + row * TP + ch * 16);
;         const f32x4 g0 = *(const f32x4*)(a.gain + 8 * ch), g1 = *(const f32x4*)(a.gain + 8 * ch + 4);
;         float yv[8] = {bf_lo(y.x), bf_hi(y.x), bf_lo(y.y), bf_hi(y.y), bf_lo(y.z), bf_hi(y.z), bf_lo(y.w), bf_hi(y.w)};
;         float gv[8];
;         if (MLSTM) { const u32x4 g = *(const u32x4*)(a.G + (size_t)row * a.ldg + 8 * ch);
;             gv[0] = bf_lo(g.x); gv[1] = bf_hi(g.x); gv[2] = bf_lo(g.y); gv[3] = bf_hi(g.y); gv[4] = bf_lo(g.z); gv[5] = bf_hi(g.z); gv[6] = bf_lo(g.w); gv[7] = bf_hi(g.w); }
;         else { const u32x2 g = *(const u32x2*)(a.G8 + (size_t)row * a.ldg8 + 8 * ch);
;             const f32x2 e0 = __builtin_amdgcn_cvt_pk_f32_fp8((int)g.x, false), e1 = __builtin_amdgcn_cvt_pk_f32_fp8((int)g.x, true), e2 = __builtin_amdgcn_cvt_pk_f32_fp8((int)g.y, false), e3 = __builtin_amdgcn_cvt_pk_f32_fp8((int)g.y, true);
;             gv[0] = e0[0] * a.g8inv; gv[1] = e0[1] * a.g8inv; gv[2] = e1[0] * a.g8inv; gv[3] = e1[1] * a.g8inv; gv[4] = e2[0] * a.g8inv; gv[5] = e2[1] * a.g8inv; gv[6] = e3[0] * a.g8inv; gv[7] = e3[1] * a.g8inv; }
;         float gn[8] = {g0[0], g0[1], g0[2], g0[3], g1[0], g1[1], g1[2], g1[3]};
;         float ov[8];
; #pragma unroll
;         for (int i = 0; i < 8; ++i) ov[i] = yv[i] * gn[i] * (MLSTM ? sigmoidf_(gv[i]) : siluf_(gv[i]));
;         u32x2 w; w.x = pg8::pk4_fp8c(ov[0] * a.oscale, ov[1] * a.oscale, ov[2] * a.oscale, ov[3] * a.oscale); w.y = pg8::pk4_fp8c(ov[4] * a.oscale, ov[5] * a.oscale, ov[6] * a.oscale, ov[7] * a.oscale);
;         *(u32x2*)(a.Out + (size_t)row * a.ldo + 8 * ch) = w; }
.Ldloop1b:
	v_pk_mul_f32 v[10:11], v[40:41], v[10:11]
	v_pk_mul_f32 v[12:13], v[42:43], v[12:13]
	v_pk_mul_f32 v[14:15], v[44:45], v[14:15]
	v_pk_mul_f32 v[16:17], v[46:47], v[16:17]
	v_pk_mul_f32 v[32:33], v[32:33], v[162:163]
	v_pk_mul_f32 v[34:35], v[34:35], v[162:163]
	v_pk_mul_f32 v[36:37], v[36:37], v[162:163]
	v_pk_mul_f32 v[38:39], v[38:39], v[162:163]
	v_pk_mul_f32 v[48:49], v[32:33], s[98:99] op_sel_hi:[1,0]
	v_pk_mul_f32 v[50:51], v[34:35], s[98:99] op_sel_hi:[1,0]
	v_pk_mul_f32 v[52:53], v[36:37], s[98:99] op_sel_hi:[1,0]
	v_pk_mul_f32 v[54:55], v[38:39], s[98:99] op_sel_hi:[1,0]
	v_exp_f32_e32 v48, v48
	v_exp_f32_e32 v49, v49
	v_exp_f32_e32 v50, v50
	v_exp_f32_e32 v51, v51
	v_exp_f32_e32 v52, v52
	v_exp_f32_e32 v53, v53
	v_exp_f32_e32 v54, v54
	v_exp_f32_e32 v55, v55
	v_pk_add_f32 v[48:49], v[48:49], 1.0 op_sel_hi:[1,0]
	v_pk_add_f32 v[50:51], v[50:51], 1.0 op_sel_hi:[1,0]
	v_pk_add_f32 v[52:53], v[52:53], 1.0 op_sel_hi:[1,0]
	v_pk_add_f32 v[54:55], v[54:55], 1.0 op_sel_hi:[1,0]
	v_rcp_f32_e32 v56, v48
	v_rcp_f32_e32 v57, v49
	v_rcp_f32_e32 v58, v50
	v_rcp_f32_e32 v59, v51
	v_rcp_f32_e32 v60, v52
	v_rcp_f32_e32 v61, v53
	v_rcp_f32_e32 v62, v54
	v_rcp_f32_e32 v63, v55
	v_pk_fma_f32 v[8:9], v[48:49], v[56:57], 1.0 op_sel_hi:[1,1,0] neg_lo:[1,0,0] neg_hi:[1,0,0]
	v_pk_fma_f32 v[18:19], v[50:51], v[58:59], 1.0 op_sel_hi:[1,1,0] neg_lo:[1,0,0] neg_hi:[1,0,0]
	v_pk_fma_f32 v[20:21], v[52:53], v[60:61], 1.0 op_sel_hi:[1,1,0] neg_lo:[1,0,0] neg_hi:[1,0,0]
	v_pk_fma_f32 v[26:27], v[54:55], v[62:63], 1.0 op_sel_hi:[1,1,0] neg_lo:[1,0,0] neg_hi:[1,0,0]
	v_pk_fma_f32 v[56:57], v[8:9], v[56:57], v[56:57]
	v_pk_fma_f32 v[58:59], v[18:19], v[58:59], v[58:59]
	v_pk_fma_f32 v[60:61], v[20:21], v[60:61], v[60:61]
	v_pk_fma_f32 v[62:63], v[26:27], v[62:63], v[62:63]
	v_pk_mul_f32 v[64:65], v[32:33], v[56:57]
	v_pk_mul_f32 v[66:67], v[34:35], v[58:59]
	v_pk_mul_f32 v[68:69], v[36:37], v[60:61]
	v_pk_mul_f32 v[70:71], v[38:39], v[62:63]
	v_pk_fma_f32 v[8:9], v[48:49], v[64:65], v[32:33] neg_lo:[1,0,0] neg_hi:[1,0,0]
	v_pk_fma_f32 v[18:19], v[50:51], v[66:67], v[34:35] neg_lo:[1,0,0] neg_hi:[1,0,0]
	v_pk_fma_f32 v[20:21], v[52:53], v[68:69], v[36:37] neg_lo:[1,0,0] neg_hi:[1,0,0]
	v_pk_fma_f32 v[26:27], v[54:55], v[70:71], v[38:39] neg_lo:[1,0,0] neg_hi:[1,0,0]
	v_pk_fma_f32 v[64:65], v[8:9], v[56:57], v[64:65]
	v_pk_fma_f32 v[66:67], v[18:19], v[58:59], v[66:67]
	v_pk_fma_f32 v[68:69], v[20:21], v[60:61], v[68:69]
	v_pk_fma_f32 v[70:71], v[26:27], v[62:63], v[70:71]
	v_pk_fma_f32 v[8:9], v[48:49], v[64:65], v[32:33] neg_lo:[1,0,0] neg_hi:[1,0,0]
	v_pk_fma_f32 v[18:19], v[50:51], v[66:67], v[34:35] neg_lo:[1,0,0] neg_hi:[1,0,0]
	v_pk_fma_f32 v[20:21], v[52:53], v[68:69], v[36:37] neg_lo:[1,0,0] neg_hi:[1,0,0]
	v_pk_fma_f32 v[26:27], v[54:55], v[70:71], v[38:39] neg_lo:[1,0,0] neg_hi:[1,0,0]
	v_pk_fma_f32 v[8:9], v[8:9], v[56:57], v[64:65]
	v_pk_fma_f32 v[18:19], v[18:19], v[58:59], v[66:67]
	v_pk_fma_f32 v[20:21], v[20:21], v[60:61], v[68:69]
	v_pk_fma_f32 v[26:27], v[26:27], v[62:63], v[70:71]
	v_div_fixup_f32 v8, v8, v48, v32
	v_div_fixup_f32 v9, v9, v49, v33
	v_div_fixup_f32 v18, v18, v50, v34
	v_div_fixup_f32 v19, v19, v51, v35
	v_div_fixup_f32 v20, v20, v52, v36
	v_div_fixup_f32 v21, v21, v53, v37
	v_div_fixup_f32 v26, v26, v54, v38
	v_div_fixup_f32 v27, v27, v55, v39
	v_pk_mul_f32 v[10:11], v[10:11], v[8:9]
	v_pk_mul_f32 v[12:13], v[12:13], v[18:19]
	v_pk_mul_f32 v[14:15], v[14:15], v[20:21]
	v_pk_mul_f32 v[16:17], v[16:17], v[26:27]
	v_pk_mul_f32 v[10:11], v[10:11], s[100:101] op_sel_hi:[1,0]
	v_pk_mul_f32 v[12:13], v[12:13], s[100:101] op_sel_hi:[1,0]
	v_pk_mul_f32 v[14:15], v[14:15], s[100:101] op_sel_hi:[1,0]
	v_pk_mul_f32 v[16:17], v[16:17], s[100:101] op_sel_hi:[1,0]
	v_med3_f32 v10, v10, s91, v231
	v_med3_f32 v11, v11, s91, v231
	v_med3_f32 v12, v12, s91, v231
	v_med3_f32 v13, v13, s91, v231
	v_med3_f32 v14, v14, s91, v231
	v_med3_f32 v15, v15, s91, v231
	v_med3_f32 v16, v16, s91, v231
	v_med3_f32 v17, v17, s91, v231
	v_cvt_pk_fp8_f32 v24, v10, v11
	v_cvt_pk_fp8_f32 v25, v14, v15
	s_nop 0
	v_cvt_pk_fp8_f32 v24, v12, v13 op_sel:[0,0,1]
	v_cvt_pk_fp8_f32 v25, v16, v17 op_sel:[0,0,1]
	s_nop 0
	global_store_dwordx2 v5, v[24:25], s[42:43]
	v_add_u32_e32 v5, 0x4000, v5
	s_add_i32 s44, s44, -1
	s_cmp_lg_u32 s44, 0
	s_cbranch_scc1 .Ldloop1
	s_waitcnt lgkmcnt(0)
	s_branch .LBB0_4301
